# speedup vs baseline: 1.0111x; 1.0081x over previous
.LBB0_43:
	v_cndmask_b32_e64 v32, v30, v29, s[18:19]
	v_ashrrev_i32_e32 v33, 31, v32
	v_lshlrev_b64 v[32:33], 10, v[32:33]
	v_fma_mixlo_f16 v31, v18, s78, 0
	v_lshl_or_b32 v32, v4, 1, v32
	v_fma_mixlo_f16 v18, v18, s78, -v31 op_sel_hi:[0,0,1]
	s_waitcnt lgkmcnt(0)
	v_lshl_add_u64 v[34:35], s[24:25], 0, v[32:33]
	v_lshl_add_u64 v[32:33], s[26:27], 0, v[32:33]
	global_store_short v[34:35], v31, off sc1
	global_store_short v[32:33], v18, off sc1
	s_andn2_b64 vcc, exec, s[34:35]
	s_cbranch_vccnz .LBB0_29
.LBB0_44:
	v_add_u32_e32 v18, 1, v29
	v_fma_mixlo_f16 v31, v19, s78, 0
	v_cndmask_b32_e64 v18, v30, v18, s[18:19]
	v_fma_mixlo_f16 v34, v19, s78, -v31 op_sel_hi:[0,0,1]
	v_ashrrev_i32_e32 v19, 31, v18
	v_lshlrev_b64 v[18:19], 10, v[18:19]
	v_lshl_or_b32 v18, v4, 1, v18
	s_waitcnt lgkmcnt(0)
	v_lshl_add_u64 v[32:33], s[24:25], 0, v[18:19]
	v_lshl_add_u64 v[18:19], s[26:27], 0, v[18:19]
	global_store_short v[32:33], v31, off sc1
	global_store_short v[18:19], v34, off sc1
	s_andn2_b64 vcc, exec, s[36:37]
	s_cbranch_vccnz .LBB0_30
.LBB0_45:
	v_add_u32_e32 v18, 2, v29
	v_cndmask_b32_e64 v18, v30, v18, s[18:19]
	v_ashrrev_i32_e32 v19, 31, v18
	v_lshlrev_b64 v[18:19], 10, v[18:19]
	v_fma_mixlo_f16 v31, v16, s78, 0
	v_lshl_or_b32 v18, v4, 1, v18
	v_fma_mixlo_f16 v16, v16, s78, -v31 op_sel_hi:[0,0,1]
	s_waitcnt lgkmcnt(0)
	v_lshl_add_u64 v[32:33], s[24:25], 0, v[18:19]
	v_lshl_add_u64 v[18:19], s[26:27], 0, v[18:19]
	global_store_short v[32:33], v31, off sc1
	global_store_short v[18:19], v16, off sc1
	s_andn2_b64 vcc, exec, s[38:39]
	s_cbranch_vccnz .LBB0_31
.LBB0_46:
	v_add_u32_e32 v16, 3, v29
	v_fma_mixlo_f16 v31, v17, s78, 0
	v_cndmask_b32_e64 v16, v30, v16, s[18:19]
	v_fma_mixlo_f16 v32, v17, s78, -v31 op_sel_hi:[0,0,1]
	v_ashrrev_i32_e32 v17, 31, v16
	v_lshlrev_b64 v[16:17], 10, v[16:17]
	v_lshl_or_b32 v16, v4, 1, v16
	s_waitcnt lgkmcnt(0)
	v_lshl_add_u64 v[18:19], s[24:25], 0, v[16:17]
	v_lshl_add_u64 v[16:17], s[26:27], 0, v[16:17]
	global_store_short v[18:19], v31, off sc1
	global_store_short v[16:17], v32, off sc1
	s_andn2_b64 vcc, exec, s[40:41]
	s_cbranch_vccnz .LBB0_32
.LBB0_47:
	v_add_u32_e32 v16, 4, v29
	v_cndmask_b32_e64 v16, v30, v16, s[18:19]
	v_ashrrev_i32_e32 v17, 31, v16
	v_lshlrev_b64 v[16:17], 10, v[16:17]
	v_fma_mixlo_f16 v31, v14, s78, 0
	v_lshl_or_b32 v16, v4, 1, v16
	v_fma_mixlo_f16 v14, v14, s78, -v31 op_sel_hi:[0,0,1]
	s_waitcnt lgkmcnt(0)
	v_lshl_add_u64 v[18:19], s[24:25], 0, v[16:17]
	v_lshl_add_u64 v[16:17], s[26:27], 0, v[16:17]
	global_store_short v[18:19], v31, off sc1
	global_store_short v[16:17], v14, off sc1
	s_andn2_b64 vcc, exec, s[42:43]
	s_cbranch_vccnz .LBB0_33
.LBB0_48:
	v_add_u32_e32 v14, 5, v29
	v_fma_mixlo_f16 v18, v15, s78, 0
	v_cndmask_b32_e64 v14, v30, v14, s[18:19]
	v_fma_mixlo_f16 v19, v15, s78, -v18 op_sel_hi:[0,0,1]
	v_ashrrev_i32_e32 v15, 31, v14
	v_lshlrev_b64 v[14:15], 10, v[14:15]
	v_lshl_or_b32 v14, v4, 1, v14
	s_waitcnt lgkmcnt(0)
	v_lshl_add_u64 v[16:17], s[24:25], 0, v[14:15]
	v_lshl_add_u64 v[14:15], s[26:27], 0, v[14:15]
	global_store_short v[16:17], v18, off sc1
	global_store_short v[14:15], v19, off sc1
	s_andn2_b64 vcc, exec, s[44:45]
	s_cbranch_vccnz .LBB0_34
.LBB0_49:
	v_add_u32_e32 v14, 6, v29
	v_cndmask_b32_e64 v14, v30, v14, s[18:19]
	v_ashrrev_i32_e32 v15, 31, v14
	v_lshlrev_b64 v[14:15], 10, v[14:15]
	v_fma_mixlo_f16 v18, v12, s78, 0
	v_lshl_or_b32 v14, v4, 1, v14
	v_fma_mixlo_f16 v12, v12, s78, -v18 op_sel_hi:[0,0,1]
	s_waitcnt lgkmcnt(0)
	v_lshl_add_u64 v[16:17], s[24:25], 0, v[14:15]
	v_lshl_add_u64 v[14:15], s[26:27], 0, v[14:15]
	global_store_short v[16:17], v18, off sc1
	global_store_short v[14:15], v12, off sc1
	s_andn2_b64 vcc, exec, s[46:47]
	s_cbranch_vccnz .LBB0_35
.LBB0_50:
	v_add_u32_e32 v12, 7, v29
	v_fma_mixlo_f16 v16, v13, s78, 0
	v_cndmask_b32_e64 v12, v30, v12, s[18:19]
	v_fma_mixlo_f16 v17, v13, s78, -v16 op_sel_hi:[0,0,1]
	v_ashrrev_i32_e32 v13, 31, v12
	v_lshlrev_b64 v[12:13], 10, v[12:13]
	v_lshl_or_b32 v12, v4, 1, v12
	s_waitcnt lgkmcnt(0)
	v_lshl_add_u64 v[14:15], s[24:25], 0, v[12:13]
	v_lshl_add_u64 v[12:13], s[26:27], 0, v[12:13]
	global_store_short v[14:15], v16, off sc1
	global_store_short v[12:13], v17, off sc1
	s_andn2_b64 vcc, exec, s[48:49]
	s_cbranch_vccnz .LBB0_36
.LBB0_51:
	v_add_u32_e32 v12, 8, v29
	v_cndmask_b32_e64 v12, v30, v12, s[18:19]
	v_ashrrev_i32_e32 v13, 31, v12
	v_lshlrev_b64 v[12:13], 10, v[12:13]
	v_fma_mixlo_f16 v16, v10, s78, 0
	v_lshl_or_b32 v12, v4, 1, v12
	v_fma_mixlo_f16 v10, v10, s78, -v16 op_sel_hi:[0,0,1]
	s_waitcnt lgkmcnt(0)
	v_lshl_add_u64 v[14:15], s[24:25], 0, v[12:13]
	v_lshl_add_u64 v[12:13], s[26:27], 0, v[12:13]
	global_store_short v[14:15], v16, off sc1
	global_store_short v[12:13], v10, off sc1
	s_andn2_b64 vcc, exec, s[50:51]
	s_cbranch_vccnz .LBB0_37
.LBB0_52:
	v_add_u32_e32 v10, 9, v29
	v_fma_mixlo_f16 v14, v11, s78, 0
	v_cndmask_b32_e64 v10, v30, v10, s[18:19]
	v_fma_mixlo_f16 v15, v11, s78, -v14 op_sel_hi:[0,0,1]
	v_ashrrev_i32_e32 v11, 31, v10
	v_lshlrev_b64 v[10:11], 10, v[10:11]
	v_lshl_or_b32 v10, v4, 1, v10
	s_waitcnt lgkmcnt(0)
	v_lshl_add_u64 v[12:13], s[24:25], 0, v[10:11]
	v_lshl_add_u64 v[10:11], s[26:27], 0, v[10:11]
	global_store_short v[12:13], v14, off sc1
	global_store_short v[10:11], v15, off sc1
	s_andn2_b64 vcc, exec, s[52:53]
	s_cbranch_vccnz .LBB0_38
.LBB0_53:
	v_add_u32_e32 v10, 10, v29
	v_cndmask_b32_e64 v10, v30, v10, s[18:19]
	v_ashrrev_i32_e32 v11, 31, v10
	v_lshlrev_b64 v[10:11], 10, v[10:11]
	v_fma_mixlo_f16 v14, v8, s78, 0
	v_lshl_or_b32 v10, v4, 1, v10
	v_fma_mixlo_f16 v8, v8, s78, -v14 op_sel_hi:[0,0,1]
	s_waitcnt lgkmcnt(0)
	v_lshl_add_u64 v[12:13], s[24:25], 0, v[10:11]
	v_lshl_add_u64 v[10:11], s[26:27], 0, v[10:11]
	global_store_short v[12:13], v14, off sc1
	global_store_short v[10:11], v8, off sc1
	s_andn2_b64 vcc, exec, s[54:55]
	s_cbranch_vccnz .LBB0_39
.LBB0_54:
	v_add_u32_e32 v8, 11, v29
	v_fma_mixlo_f16 v12, v9, s78, 0
	v_cndmask_b32_e64 v8, v30, v8, s[18:19]
	v_fma_mixlo_f16 v13, v9, s78, -v12 op_sel_hi:[0,0,1]
	v_ashrrev_i32_e32 v9, 31, v8
	v_lshlrev_b64 v[8:9], 10, v[8:9]
	v_lshl_or_b32 v8, v4, 1, v8
	s_waitcnt lgkmcnt(0)
	v_lshl_add_u64 v[10:11], s[24:25], 0, v[8:9]
	v_lshl_add_u64 v[8:9], s[26:27], 0, v[8:9]
	global_store_short v[10:11], v12, off sc1
	global_store_short v[8:9], v13, off sc1
	s_andn2_b64 vcc, exec, s[56:57]
	s_cbranch_vccnz .LBB0_40
.LBB0_55:
	v_add_u32_e32 v8, 12, v29
	v_cndmask_b32_e64 v8, v30, v8, s[18:19]
	v_ashrrev_i32_e32 v9, 31, v8
	v_lshlrev_b64 v[8:9], 10, v[8:9]
	v_fma_mixlo_f16 v12, v6, s78, 0
	v_lshl_or_b32 v8, v4, 1, v8
	v_fma_mixlo_f16 v6, v6, s78, -v12 op_sel_hi:[0,0,1]
	s_waitcnt lgkmcnt(0)
	v_lshl_add_u64 v[10:11], s[24:25], 0, v[8:9]
	v_lshl_add_u64 v[8:9], s[26:27], 0, v[8:9]
	global_store_short v[10:11], v12, off sc1
	global_store_short v[8:9], v6, off sc1
	s_andn2_b64 vcc, exec, s[58:59]
	s_cbranch_vccnz .LBB0_41
.LBB0_56:
	v_add_u32_e32 v6, 13, v29
	v_fma_mixlo_f16 v10, v7, s78, 0
	v_cndmask_b32_e64 v6, v30, v6, s[18:19]
	v_fma_mixlo_f16 v11, v7, s78, -v10 op_sel_hi:[0,0,1]
	v_ashrrev_i32_e32 v7, 31, v6
	v_lshlrev_b64 v[6:7], 10, v[6:7]
	v_lshl_or_b32 v6, v4, 1, v6
	s_waitcnt lgkmcnt(0)
	v_lshl_add_u64 v[8:9], s[24:25], 0, v[6:7]
	v_lshl_add_u64 v[6:7], s[26:27], 0, v[6:7]
	global_store_short v[8:9], v10, off sc1
	global_store_short v[6:7], v11, off sc1
	s_andn2_b64 vcc, exec, s[60:61]
	s_cbranch_vccnz .LBB0_42
.LBB0_57:
	v_add_u32_e32 v6, 14, v29
	v_cndmask_b32_e64 v6, v30, v6, s[18:19]
	v_ashrrev_i32_e32 v7, 31, v6
	v_lshlrev_b64 v[6:7], 10, v[6:7]
	v_fma_mixlo_f16 v10, v0, s78, 0
	v_lshl_or_b32 v6, v4, 1, v6
	v_fma_mixlo_f16 v0, v0, s78, -v10 op_sel_hi:[0,0,1]
	s_waitcnt lgkmcnt(0)
	v_lshl_add_u64 v[8:9], s[24:25], 0, v[6:7]
	v_lshl_add_u64 v[6:7], s[26:27], 0, v[6:7]
	global_store_short v[8:9], v10, off sc1
	global_store_short v[6:7], v0, off sc1
	s_andn2_b64 vcc, exec, s[22:23]
	s_cbranch_vccnz .LBB0_6
.LBB0_58:
	v_add_u32_e32 v0, 15, v29
	v_fma_mixlo_f16 v8, v1, s78, 0
	v_cndmask_b32_e64 v0, v30, v0, s[18:19]
	v_fma_mixlo_f16 v9, v1, s78, -v8 op_sel_hi:[0,0,1]
	v_ashrrev_i32_e32 v1, 31, v0
	v_lshlrev_b64 v[0:1], 10, v[0:1]
	v_lshl_or_b32 v0, v4, 1, v0
	s_waitcnt lgkmcnt(0)
	v_lshl_add_u64 v[6:7], s[24:25], 0, v[0:1]
	v_lshl_add_u64 v[0:1], s[26:27], 0, v[0:1]
	global_store_short v[6:7], v8, off sc1
	global_store_short v[0:1], v9, off sc1
	s_branch .LBB0_6

.LBB4_31:
	s_cmp_eq_u32 s22, 0
	s_cselect_b64 s[0:1], -1, 0
	s_lshl_b32 s3, s3, 6
	s_ashr_i32 s5, s3, 31
	s_cmp_lt_i32 s21, 1
	s_cselect_b64 s[6:7], -1, 0
	s_and_b64 s[6:7], s[6:7], s[28:29]
	s_mul_i32 s4, s20, s2
	v_or_b32_e32 v0, s3, v0
	v_mov_b32_e32 v1, s5
	s_and_b64 vcc, exec, s[6:7]
	s_cbranch_vccz .LBB4_33
	s_and_b64 s[6:7], s[0:1], exec
	s_cselect_b32 s6, s4, s2
	s_ashr_i32 s7, s6, 31
	s_lshl_b64 s[6:7], s[6:7], 9
	s_mov_b32 s3, 0x43800000
	v_lshl_add_u64 v[18:19], v[0:1], 0, s[6:7]
	v_fma_mixlo_f16 v22, v16, s3, 0
	v_lshlrev_b64 v[18:19], 1, v[18:19]
	v_fma_mixlo_f16 v16, v16, s3, -v22 op_sel_hi:[0,0,1]
	v_lshl_add_u64 v[20:21], s[24:25], 0, v[18:19]
	v_lshl_add_u64 v[18:19], s[26:27], 0, v[18:19]
	global_store_short v[20:21], v22, off sc1
	global_store_short v[18:19], v16, off sc1
.LBB4_33:
	s_cmp_gt_i32 s21, 1
	s_cselect_b64 s[6:7], -1, 0
	s_cmp_lt_i32 s20, 2
	s_cselect_b64 s[8:9], -1, 0
	s_or_b64 s[6:7], s[6:7], s[8:9]
	s_and_b64 vcc, exec, s[6:7]
	s_cbranch_vccnz .LBB4_35
	s_mov_b32 s3, 0x43800000
	v_fma_mixlo_f16 v20, v17, s3, 0
	v_fma_mixlo_f16 v21, v17, s3, -v20 op_sel_hi:[0,0,1]
	s_add_i32 s3, s4, 1
	s_and_b64 s[6:7], s[0:1], exec
	s_cselect_b32 s6, s3, s2
	s_ashr_i32 s7, s6, 31
	s_lshl_b64 s[6:7], s[6:7], 9
	v_lshl_add_u64 v[16:17], v[0:1], 0, s[6:7]
	v_lshlrev_b64 v[16:17], 1, v[16:17]
	v_lshl_add_u64 v[18:19], s[24:25], 0, v[16:17]
	v_lshl_add_u64 v[16:17], s[26:27], 0, v[16:17]
	global_store_short v[18:19], v20, off sc1
	global_store_short v[16:17], v21, off sc1
.LBB4_35:
	s_cmp_gt_i32 s21, 2
	s_cselect_b64 s[6:7], -1, 0
	s_cmp_lt_i32 s20, 3
	s_cselect_b64 s[8:9], -1, 0
	s_or_b64 s[6:7], s[6:7], s[8:9]
	s_and_b64 vcc, exec, s[6:7]
	s_cbranch_vccnz .LBB4_37
	s_mov_b32 s3, 0x43800000
	v_fma_mixlo_f16 v20, v14, s3, 0
	v_fma_mixlo_f16 v14, v14, s3, -v20 op_sel_hi:[0,0,1]
	s_add_i32 s3, s4, 2
	s_and_b64 s[6:7], s[0:1], exec
	s_cselect_b32 s6, s3, s2
	s_ashr_i32 s7, s6, 31
	s_lshl_b64 s[6:7], s[6:7], 9
	v_lshl_add_u64 v[16:17], v[0:1], 0, s[6:7]
	v_lshlrev_b64 v[16:17], 1, v[16:17]
	v_lshl_add_u64 v[18:19], s[24:25], 0, v[16:17]
	v_lshl_add_u64 v[16:17], s[26:27], 0, v[16:17]
	global_store_short v[18:19], v20, off sc1
	global_store_short v[16:17], v14, off sc1
.LBB4_37:
	s_cmp_gt_i32 s21, 3
	s_cselect_b64 s[6:7], -1, 0
	s_cmp_lt_i32 s20, 4
	s_cselect_b64 s[8:9], -1, 0
	s_or_b64 s[6:7], s[6:7], s[8:9]
	s_and_b64 vcc, exec, s[6:7]
	s_cbranch_vccnz .LBB4_39
	s_mov_b32 s3, 0x43800000
	v_fma_mixlo_f16 v18, v15, s3, 0
	v_fma_mixlo_f16 v19, v15, s3, -v18 op_sel_hi:[0,0,1]
	s_add_i32 s3, s4, 3
	s_and_b64 s[6:7], s[0:1], exec
	s_cselect_b32 s6, s3, s2
	s_ashr_i32 s7, s6, 31
	s_lshl_b64 s[6:7], s[6:7], 9
	v_lshl_add_u64 v[14:15], v[0:1], 0, s[6:7]
	v_lshlrev_b64 v[14:15], 1, v[14:15]
	v_lshl_add_u64 v[16:17], s[24:25], 0, v[14:15]
	v_lshl_add_u64 v[14:15], s[26:27], 0, v[14:15]
	global_store_short v[16:17], v18, off sc1
	global_store_short v[14:15], v19, off sc1
.LBB4_39:
	s_cmp_gt_i32 s21, 4
	s_cselect_b64 s[6:7], -1, 0
	s_cmp_lt_i32 s20, 5
	s_cselect_b64 s[8:9], -1, 0
	s_or_b64 s[6:7], s[6:7], s[8:9]
	s_and_b64 vcc, exec, s[6:7]
	s_cbranch_vccnz .LBB4_41
	s_mov_b32 s3, 0x43800000
	v_fma_mixlo_f16 v18, v12, s3, 0
	v_fma_mixlo_f16 v12, v12, s3, -v18 op_sel_hi:[0,0,1]
	s_add_i32 s3, s4, 4
	s_and_b64 s[6:7], s[0:1], exec
	s_cselect_b32 s6, s3, s2
	s_ashr_i32 s7, s6, 31
	s_lshl_b64 s[6:7], s[6:7], 9
	v_lshl_add_u64 v[14:15], v[0:1], 0, s[6:7]
	v_lshlrev_b64 v[14:15], 1, v[14:15]
	v_lshl_add_u64 v[16:17], s[24:25], 0, v[14:15]
	v_lshl_add_u64 v[14:15], s[26:27], 0, v[14:15]
	global_store_short v[16:17], v18, off sc1
	global_store_short v[14:15], v12, off sc1
.LBB4_41:
	s_cmp_gt_i32 s21, 5
	s_cselect_b64 s[6:7], -1, 0
	s_cmp_lt_i32 s20, 6
	s_cselect_b64 s[8:9], -1, 0
	s_or_b64 s[6:7], s[6:7], s[8:9]
	s_and_b64 vcc, exec, s[6:7]
	s_cbranch_vccnz .LBB4_43
	s_mov_b32 s3, 0x43800000
	v_fma_mixlo_f16 v16, v13, s3, 0
	v_fma_mixlo_f16 v17, v13, s3, -v16 op_sel_hi:[0,0,1]
	s_add_i32 s3, s4, 5
	s_and_b64 s[6:7], s[0:1], exec
	s_cselect_b32 s6, s3, s2
	s_ashr_i32 s7, s6, 31
	s_lshl_b64 s[6:7], s[6:7], 9
	v_lshl_add_u64 v[12:13], v[0:1], 0, s[6:7]
	v_lshlrev_b64 v[12:13], 1, v[12:13]
	v_lshl_add_u64 v[14:15], s[24:25], 0, v[12:13]
	v_lshl_add_u64 v[12:13], s[26:27], 0, v[12:13]
	global_store_short v[14:15], v16, off sc1
	global_store_short v[12:13], v17, off sc1
.LBB4_43:
	s_cmp_gt_i32 s21, 6
	s_cselect_b64 s[6:7], -1, 0
	s_cmp_lt_i32 s20, 7
	s_cselect_b64 s[8:9], -1, 0
	s_or_b64 s[6:7], s[6:7], s[8:9]
	s_and_b64 vcc, exec, s[6:7]
	s_cbranch_vccnz .LBB4_45
	s_mov_b32 s3, 0x43800000
	v_fma_mixlo_f16 v16, v10, s3, 0
	v_fma_mixlo_f16 v10, v10, s3, -v16 op_sel_hi:[0,0,1]
	s_add_i32 s3, s4, 6
	s_and_b64 s[6:7], s[0:1], exec
	s_cselect_b32 s6, s3, s2
	s_ashr_i32 s7, s6, 31
	s_lshl_b64 s[6:7], s[6:7], 9
	v_lshl_add_u64 v[12:13], v[0:1], 0, s[6:7]
	v_lshlrev_b64 v[12:13], 1, v[12:13]
	v_lshl_add_u64 v[14:15], s[24:25], 0, v[12:13]
	v_lshl_add_u64 v[12:13], s[26:27], 0, v[12:13]
	global_store_short v[14:15], v16, off sc1
	global_store_short v[12:13], v10, off sc1
.LBB4_45:
	s_cmp_gt_i32 s21, 7
	s_cselect_b64 s[6:7], -1, 0
	s_cmp_lt_i32 s20, 8
	s_cselect_b64 s[8:9], -1, 0
	s_or_b64 s[6:7], s[6:7], s[8:9]
	s_and_b64 vcc, exec, s[6:7]
	s_cbranch_vccnz .LBB4_47
	s_mov_b32 s3, 0x43800000
	v_fma_mixlo_f16 v14, v11, s3, 0
	v_fma_mixlo_f16 v15, v11, s3, -v14 op_sel_hi:[0,0,1]
	s_add_i32 s3, s4, 7
	s_and_b64 s[6:7], s[0:1], exec
	s_cselect_b32 s6, s3, s2
	s_ashr_i32 s7, s6, 31
	s_lshl_b64 s[6:7], s[6:7], 9
	v_lshl_add_u64 v[10:11], v[0:1], 0, s[6:7]
	v_lshlrev_b64 v[10:11], 1, v[10:11]
	v_lshl_add_u64 v[12:13], s[24:25], 0, v[10:11]
	v_lshl_add_u64 v[10:11], s[26:27], 0, v[10:11]
	global_store_short v[12:13], v14, off sc1
	global_store_short v[10:11], v15, off sc1
.LBB4_47:
	s_cmp_gt_i32 s21, 8
	s_cselect_b64 s[6:7], -1, 0
	s_cmp_lt_i32 s20, 9
	s_cselect_b64 s[8:9], -1, 0
	s_or_b64 s[6:7], s[6:7], s[8:9]
	s_and_b64 vcc, exec, s[6:7]
	s_cbranch_vccnz .LBB4_49
	s_mov_b32 s3, 0x43800000
	v_fma_mixlo_f16 v14, v8, s3, 0
	v_fma_mixlo_f16 v8, v8, s3, -v14 op_sel_hi:[0,0,1]
	s_add_i32 s3, s4, 8
	s_and_b64 s[6:7], s[0:1], exec
	s_cselect_b32 s6, s3, s2
	s_ashr_i32 s7, s6, 31
	s_lshl_b64 s[6:7], s[6:7], 9
	v_lshl_add_u64 v[10:11], v[0:1], 0, s[6:7]
	v_lshlrev_b64 v[10:11], 1, v[10:11]
	v_lshl_add_u64 v[12:13], s[24:25], 0, v[10:11]
	v_lshl_add_u64 v[10:11], s[26:27], 0, v[10:11]
	global_store_short v[12:13], v14, off sc1
	global_store_short v[10:11], v8, off sc1
.LBB4_49:
	s_cmp_gt_i32 s21, 9
	s_cselect_b64 s[6:7], -1, 0
	s_cmp_lt_i32 s20, 10
	s_cselect_b64 s[8:9], -1, 0
	s_or_b64 s[6:7], s[6:7], s[8:9]
	s_and_b64 vcc, exec, s[6:7]
	s_cbranch_vccnz .LBB4_51
	s_mov_b32 s3, 0x43800000
	v_fma_mixlo_f16 v12, v9, s3, 0
	v_fma_mixlo_f16 v13, v9, s3, -v12 op_sel_hi:[0,0,1]
	s_add_i32 s3, s4, 9
	s_and_b64 s[6:7], s[0:1], exec
	s_cselect_b32 s6, s3, s2
	s_ashr_i32 s7, s6, 31
	s_lshl_b64 s[6:7], s[6:7], 9
	v_lshl_add_u64 v[8:9], v[0:1], 0, s[6:7]
	v_lshlrev_b64 v[8:9], 1, v[8:9]
	v_lshl_add_u64 v[10:11], s[24:25], 0, v[8:9]
	v_lshl_add_u64 v[8:9], s[26:27], 0, v[8:9]
	global_store_short v[10:11], v12, off sc1
	global_store_short v[8:9], v13, off sc1
.LBB4_51:
	s_cmp_gt_i32 s21, 10
	s_cselect_b64 s[6:7], -1, 0
	s_cmp_lt_i32 s20, 11
	s_cselect_b64 s[8:9], -1, 0
	s_or_b64 s[6:7], s[6:7], s[8:9]
	s_and_b64 vcc, exec, s[6:7]
	s_cbranch_vccnz .LBB4_53
	s_mov_b32 s3, 0x43800000
	v_fma_mixlo_f16 v12, v6, s3, 0
	v_fma_mixlo_f16 v6, v6, s3, -v12 op_sel_hi:[0,0,1]
	s_add_i32 s3, s4, 10
	s_and_b64 s[6:7], s[0:1], exec
	s_cselect_b32 s6, s3, s2
	s_ashr_i32 s7, s6, 31
	s_lshl_b64 s[6:7], s[6:7], 9
	v_lshl_add_u64 v[8:9], v[0:1], 0, s[6:7]
	v_lshlrev_b64 v[8:9], 1, v[8:9]
	v_lshl_add_u64 v[10:11], s[24:25], 0, v[8:9]
	v_lshl_add_u64 v[8:9], s[26:27], 0, v[8:9]
	global_store_short v[10:11], v12, off sc1
	global_store_short v[8:9], v6, off sc1
.LBB4_53:
	s_cmp_gt_i32 s21, 11
	s_cselect_b64 s[6:7], -1, 0
	s_cmp_lt_i32 s20, 12
	s_cselect_b64 s[8:9], -1, 0
	s_or_b64 s[6:7], s[6:7], s[8:9]
	s_and_b64 vcc, exec, s[6:7]
	s_cbranch_vccnz .LBB4_55
	s_mov_b32 s3, 0x43800000
	v_fma_mixlo_f16 v10, v7, s3, 0
	v_fma_mixlo_f16 v11, v7, s3, -v10 op_sel_hi:[0,0,1]
	s_add_i32 s3, s4, 11
	s_and_b64 s[6:7], s[0:1], exec
	s_cselect_b32 s6, s3, s2
	s_ashr_i32 s7, s6, 31
	s_lshl_b64 s[6:7], s[6:7], 9
	v_lshl_add_u64 v[6:7], v[0:1], 0, s[6:7]
	v_lshlrev_b64 v[6:7], 1, v[6:7]
	v_lshl_add_u64 v[8:9], s[24:25], 0, v[6:7]
	v_lshl_add_u64 v[6:7], s[26:27], 0, v[6:7]
	global_store_short v[8:9], v10, off sc1
	global_store_short v[6:7], v11, off sc1
.LBB4_55:
	s_cmp_gt_i32 s21, 12
	s_cselect_b64 s[6:7], -1, 0
	s_cmp_lt_i32 s20, 13
	s_cselect_b64 s[8:9], -1, 0
	s_or_b64 s[6:7], s[6:7], s[8:9]
	s_and_b64 vcc, exec, s[6:7]
	s_cbranch_vccnz .LBB4_57
	s_mov_b32 s3, 0x43800000
	v_fma_mixlo_f16 v10, v4, s3, 0
	v_fma_mixlo_f16 v4, v4, s3, -v10 op_sel_hi:[0,0,1]
	s_add_i32 s3, s4, 12
	s_and_b64 s[6:7], s[0:1], exec
	s_cselect_b32 s6, s3, s2
	s_ashr_i32 s7, s6, 31
	s_lshl_b64 s[6:7], s[6:7], 9
	v_lshl_add_u64 v[6:7], v[0:1], 0, s[6:7]
	v_lshlrev_b64 v[6:7], 1, v[6:7]
	v_lshl_add_u64 v[8:9], s[24:25], 0, v[6:7]
	v_lshl_add_u64 v[6:7], s[26:27], 0, v[6:7]
	global_store_short v[8:9], v10, off sc1
	global_store_short v[6:7], v4, off sc1
.LBB4_57:
	s_cmp_gt_i32 s21, 13
	s_cselect_b64 s[6:7], -1, 0
	s_cmp_lt_i32 s20, 14
	s_cselect_b64 s[8:9], -1, 0
	s_or_b64 s[6:7], s[6:7], s[8:9]
	s_and_b64 vcc, exec, s[6:7]
	s_cbranch_vccnz .LBB4_59
	s_mov_b32 s3, 0x43800000
	v_fma_mixlo_f16 v8, v5, s3, 0
	v_fma_mixlo_f16 v9, v5, s3, -v8 op_sel_hi:[0,0,1]
	s_add_i32 s3, s4, 13
	s_and_b64 s[6:7], s[0:1], exec
	s_cselect_b32 s6, s3, s2
	s_ashr_i32 s7, s6, 31
	s_lshl_b64 s[6:7], s[6:7], 9
	v_lshl_add_u64 v[4:5], v[0:1], 0, s[6:7]
	v_lshlrev_b64 v[4:5], 1, v[4:5]
	v_lshl_add_u64 v[6:7], s[24:25], 0, v[4:5]
	v_lshl_add_u64 v[4:5], s[26:27], 0, v[4:5]
	global_store_short v[6:7], v8, off sc1
	global_store_short v[4:5], v9, off sc1
.LBB4_59:
	s_cmp_gt_i32 s21, 14
	s_cselect_b64 s[6:7], -1, 0
	s_cmp_lt_i32 s20, 15
	s_cselect_b64 s[8:9], -1, 0
	s_or_b64 s[6:7], s[6:7], s[8:9]
	s_and_b64 vcc, exec, s[6:7]
	s_cbranch_vccnz .LBB4_61
	s_mov_b32 s3, 0x43800000
	v_fma_mixlo_f16 v8, v2, s3, 0
	v_fma_mixlo_f16 v2, v2, s3, -v8 op_sel_hi:[0,0,1]
	s_add_i32 s3, s4, 14
	s_and_b64 s[6:7], s[0:1], exec
	s_cselect_b32 s6, s3, s2
	s_ashr_i32 s7, s6, 31
	s_lshl_b64 s[6:7], s[6:7], 9
	v_lshl_add_u64 v[4:5], v[0:1], 0, s[6:7]
	v_lshlrev_b64 v[4:5], 1, v[4:5]
	v_lshl_add_u64 v[6:7], s[24:25], 0, v[4:5]
	v_lshl_add_u64 v[4:5], s[26:27], 0, v[4:5]
	global_store_short v[6:7], v8, off sc1
	global_store_short v[4:5], v2, off sc1
.LBB4_61:
	s_cmp_gt_i32 s21, 15
	s_cselect_b64 s[6:7], -1, 0
	s_cmp_lt_i32 s20, 16
	s_cselect_b64 s[8:9], -1, 0
	s_or_b64 s[6:7], s[6:7], s[8:9]
	s_and_b64 vcc, exec, s[6:7]
	s_cbranch_vccnz .LBB4_63
	s_add_i32 s4, s4, 15
	s_and_b64 s[0:1], s[0:1], exec
	s_cselect_b32 s0, s4, s2
	s_ashr_i32 s1, s0, 31
	s_lshl_b64 s[0:1], s[0:1], 9
	s_mov_b32 s3, 0x43800000
	v_lshl_add_u64 v[0:1], v[0:1], 0, s[0:1]
	v_fma_mixlo_f16 v4, v3, s3, 0
	v_lshlrev_b64 v[0:1], 1, v[0:1]
	v_fma_mixlo_f16 v5, v3, s3, -v4 op_sel_hi:[0,0,1]
	v_lshl_add_u64 v[2:3], s[24:25], 0, v[0:1]
	v_lshl_add_u64 v[0:1], s[26:27], 0, v[0:1]
	global_store_short v[2:3], v4, off sc1
	global_store_short v[0:1], v5, off sc1

.LBB12_5:
	v_lshlrev_b32_e32 v0, 2, v0
	v_and_b32_e32 v58, 0xfc, v0
	v_lshlrev_b64 v[4:5], 11, v[4:5]
	v_lshlrev_b32_e32 v0, 2, v58
	v_mov_b32_e32 v1, 0
	s_waitcnt lgkmcnt(0)
	v_lshl_add_u64 v[4:5], s[24:25], 0, v[4:5]
	v_lshl_add_u64 v[4:5], v[4:5], 0, v[0:1]
	global_load_dwordx4 v[8:11], v[4:5], off
	global_load_dwordx4 v[12:15], v0, s[20:21]
	global_load_dwordx4 v[16:19], v0, s[20:21] offset:1024
	global_load_dwordx4 v[20:23], v[4:5], off offset:1024
	v_lshlrev_b64 v[4:5], 11, v[2:3]
	v_lshl_add_u64 v[24:25], s[22:23], 0, v[4:5]
	v_lshl_add_u64 v[40:41], v[24:25], 0, v[0:1]
	global_load_dwordx4 v[24:27], v[40:41], off
	global_load_dwordx4 v[28:31], v[40:41], off offset:1024
	global_load_dwordx4 v[32:35], v0, s[12:13]
	global_load_dwordx4 v[36:39], v0, s[12:13] offset:1024
	v_lshlrev_b64 v[6:7], 11, v[6:7]
	v_lshl_add_u64 v[6:7], s[18:19], 0, v[6:7]
	v_lshl_add_u64 v[52:53], v[6:7], 0, v[0:1]
	global_load_dwordx4 v[40:43], v0, s[14:15]
	global_load_dwordx4 v[44:47], v0, s[8:9]
	global_load_dwordx4 v[48:51], v0, s[10:11]
	v_mov_b32_e32 v59, 0x3727c5ac
	s_mov_b32 s12, 0xf800000
	v_mov_b32_e32 v60, 0x260
	v_lshl_add_u64 v[4:5], s[4:5], 0, v[4:5]
	v_lshlrev_b64 v[2:3], 10, v[2:3]
	s_waitcnt vmcnt(9)
	v_pk_add_f32 v[54:55], v[12:13], v[8:9]
	global_load_dwordx4 v[6:9], v0, s[14:15] offset:1024
	s_waitcnt vmcnt(8)
	v_pk_add_f32 v[20:21], v[16:17], v[20:21]
	v_pk_add_f32 v[18:19], v[18:19], v[22:23]
	v_pk_add_f32 v[56:57], v[14:15], v[10:11]
	global_load_dwordx4 v[10:13], v0, s[8:9] offset:1024
	global_load_dwordx4 v[14:17], v0, s[10:11] offset:1024
	s_waitcnt vmcnt(9)
	v_pk_add_f32 v[54:55], v[24:25], v[54:55]
	s_waitcnt vmcnt(8)
	v_pk_add_f32 v[28:29], v[28:29], v[20:21]
	v_pk_add_f32 v[30:31], v[30:31], v[18:19]
	global_load_dwordx4 v[18:21], v[52:53], off
	global_load_dwordx4 v[22:25], v[52:53], off offset:1024
	v_add_f32_e32 v52, 0, v54
	v_pk_add_f32 v[26:27], v[26:27], v[56:57]
	v_add_f32_e32 v52, v52, v55
	v_add_f32_e32 v52, v52, v26
	v_add_f32_e32 v52, v52, v27
	v_add_f32_e32 v52, v52, v28
	v_add_f32_e32 v52, v52, v29
	v_add_f32_e32 v52, v52, v30
	v_add_f32_e32 v52, v52, v31
	s_nop 1
	v_add_f32_dpp v52, v52, v52 quad_perm:[1,0,3,2] row_mask:0xf bank_mask:0xf bound_ctrl:1
	s_nop 1
	v_add_f32_dpp v52, v52, v52 quad_perm:[2,3,0,1] row_mask:0xf bank_mask:0xf bound_ctrl:1
	s_nop 1
	v_add_f32_dpp v52, v52, v52 row_half_mirror row_mask:0xf bank_mask:0xf bound_ctrl:1
	s_nop 1
	v_add_f32_dpp v52, v52, v52 row_mirror row_mask:0xf bank_mask:0xf bound_ctrl:1
	s_nop 0
	v_readlane_b32 s8, v52, 16
	v_readlane_b32 s9, v52, 48
	v_readlane_b32 s0, v52, 0
	v_readlane_b32 s1, v52, 32
	v_mov_b32_e32 v52, s8
	v_mov_b32_e32 v53, s9
	v_pk_add_f32 v[52:53], s[0:1], v[52:53]
	s_nop 0
	v_add_f32_e32 v52, v52, v53
	v_mul_f32_e32 v52, 0x3b000000, v52
	v_pk_add_f32 v[54:55], v[54:55], v[52:53] op_sel_hi:[1,0] neg_lo:[0,1] neg_hi:[0,1]
	v_pk_add_f32 v[26:27], v[26:27], v[52:53] op_sel_hi:[1,0] neg_lo:[0,1] neg_hi:[0,1]
	v_pk_add_f32 v[28:29], v[28:29], v[52:53] op_sel_hi:[1,0] neg_lo:[0,1] neg_hi:[0,1]
	v_pk_add_f32 v[30:31], v[30:31], v[52:53] op_sel_hi:[1,0] neg_lo:[0,1] neg_hi:[0,1]
	v_pk_mul_f32 v[52:53], v[54:55], v[54:55]
	s_waitcnt vmcnt(9)
	v_pk_mul_f32 v[32:33], v[32:33], v[54:55]
	v_add_f32_e32 v56, v52, v53
	v_pk_mul_f32 v[52:53], v[26:27], v[26:27]
	v_pk_mul_f32 v[26:27], v[34:35], v[26:27]
	v_add_f32_e32 v52, v56, v52
	v_add_f32_e32 v56, v52, v53
	v_pk_mul_f32 v[52:53], v[28:29], v[28:29]
	s_waitcnt vmcnt(8)
	v_pk_mul_f32 v[28:29], v[36:37], v[28:29]
	v_add_f32_e32 v52, v56, v52
	v_add_f32_e32 v56, v52, v53
	v_pk_mul_f32 v[52:53], v[30:31], v[30:31]
	v_pk_mul_f32 v[30:31], v[38:39], v[30:31]
	v_add_f32_e32 v52, v56, v52
	v_add_f32_e32 v52, v52, v53
	s_nop 1
	v_add_f32_dpp v52, v52, v52 quad_perm:[1,0,3,2] row_mask:0xf bank_mask:0xf bound_ctrl:1
	s_nop 1
	v_add_f32_dpp v52, v52, v52 quad_perm:[2,3,0,1] row_mask:0xf bank_mask:0xf bound_ctrl:1
	s_nop 1
	v_add_f32_dpp v52, v52, v52 row_half_mirror row_mask:0xf bank_mask:0xf bound_ctrl:1
	s_nop 1
	v_add_f32_dpp v52, v52, v52 row_mirror row_mask:0xf bank_mask:0xf bound_ctrl:1
	s_nop 0
	v_readlane_b32 s8, v52, 16
	v_readlane_b32 s9, v52, 48
	v_readlane_b32 s0, v52, 0
	v_readlane_b32 s1, v52, 32
	v_mov_b32_e32 v52, s8
	v_mov_b32_e32 v53, s9
	v_pk_add_f32 v[52:53], s[0:1], v[52:53]
	s_nop 0
	v_add_f32_e32 v52, v52, v53
	v_fmamk_f32 v52, v52, 0x3b000000, v59
	v_mul_f32_e32 v53, 0x4f800000, v52
	v_cmp_gt_f32_e32 vcc, s12, v52
	s_nop 1
	v_cndmask_b32_e32 v52, v52, v53, vcc
	v_sqrt_f32_e32 v53, v52
	s_nop 0
	v_add_u32_e32 v34, -1, v53
	v_add_u32_e32 v35, 1, v53
	v_fma_f32 v36, -v34, v53, v52
	v_fma_f32 v37, -v35, v53, v52
	v_cmp_ge_f32_e64 s[0:1], 0, v36
	s_nop 1
	v_cndmask_b32_e64 v34, v53, v34, s[0:1]
	v_cmp_lt_f32_e64 s[0:1], 0, v37
	s_nop 1
	v_cndmask_b32_e64 v34, v34, v35, s[0:1]
	v_mul_f32_e32 v35, 0x37800000, v34
	v_cndmask_b32_e32 v34, v34, v35, vcc
	v_cmp_class_f32_e32 vcc, v52, v60
	s_nop 1
	v_cndmask_b32_e32 v34, v34, v52, vcc
	v_div_scale_f32 v35, s[0:1], v34, v34, 1.0
	v_rcp_f32_e32 v36, v35
	v_div_scale_f32 v37, vcc, 1.0, v34, 1.0
	v_fma_f32 v38, -v35, v36, 1.0
	v_fmac_f32_e32 v36, v38, v36
	v_mul_f32_e32 v38, v37, v36
	v_fma_f32 v39, -v35, v38, v37
	v_fmac_f32_e32 v38, v39, v36
	v_fma_f32 v35, -v35, v38, v37
	v_div_fmas_f32 v35, v35, v36, v38
	v_div_fixup_f32 v34, v35, v34, 1.0
	s_waitcnt vmcnt(7)
	v_pk_fma_f32 v[32:33], v[34:35], v[32:33], v[40:41] op_sel_hi:[0,1,1]
	s_waitcnt vmcnt(4)
	v_pk_fma_f32 v[6:7], v[34:35], v[28:29], v[6:7] op_sel_hi:[0,1,1]
	s_waitcnt vmcnt(1)
	v_pk_add_f32 v[18:19], v[32:33], v[18:19]
	v_pk_fma_f32 v[26:27], v[34:35], v[26:27], v[42:43] op_sel_hi:[0,1,1]
	s_waitcnt vmcnt(0)
	v_pk_add_f32 v[6:7], v[6:7], v[22:23]
	v_add_f32_e32 v22, 0, v18
	v_pk_add_f32 v[20:21], v[26:27], v[20:21]
	v_add_f32_e32 v22, v22, v19
	v_add_f32_e32 v22, v22, v20
	v_add_f32_e32 v22, v22, v21
	v_pk_fma_f32 v[8:9], v[34:35], v[30:31], v[8:9] op_sel_hi:[0,1,1]
	v_add_f32_e32 v22, v22, v6
	v_pk_add_f32 v[8:9], v[8:9], v[24:25]
	v_add_f32_e32 v22, v22, v7
	v_add_f32_e32 v22, v22, v8
	v_add_f32_e32 v22, v22, v9
	s_nop 1
	v_add_f32_dpp v22, v22, v22 quad_perm:[1,0,3,2] row_mask:0xf bank_mask:0xf bound_ctrl:1
	s_nop 1
	v_add_f32_dpp v22, v22, v22 quad_perm:[2,3,0,1] row_mask:0xf bank_mask:0xf bound_ctrl:1
	s_nop 1
	v_add_f32_dpp v22, v22, v22 row_half_mirror row_mask:0xf bank_mask:0xf bound_ctrl:1
	s_nop 1
	v_add_f32_dpp v22, v22, v22 row_mirror row_mask:0xf bank_mask:0xf bound_ctrl:1
	s_nop 0
	v_readlane_b32 s8, v22, 16
	v_readlane_b32 s9, v22, 48
	v_readlane_b32 s0, v22, 0
	v_readlane_b32 s1, v22, 32
	v_mov_b32_e32 v22, s8
	v_mov_b32_e32 v23, s9
	v_pk_add_f32 v[22:23], s[0:1], v[22:23]
	s_nop 0
	v_add_f32_e32 v22, v22, v23
	v_mul_f32_e32 v22, 0x3b000000, v22
	v_pk_add_f32 v[18:19], v[18:19], v[22:23] op_sel_hi:[1,0] neg_lo:[0,1] neg_hi:[0,1]
	v_pk_add_f32 v[20:21], v[20:21], v[22:23] op_sel_hi:[1,0] neg_lo:[0,1] neg_hi:[0,1]
	v_pk_add_f32 v[24:25], v[6:7], v[22:23] op_sel_hi:[1,0] neg_lo:[0,1] neg_hi:[0,1]
	v_pk_mul_f32 v[6:7], v[18:19], v[18:19]
	v_pk_add_f32 v[22:23], v[8:9], v[22:23] op_sel_hi:[1,0] neg_lo:[0,1] neg_hi:[0,1]
	v_pk_mul_f32 v[8:9], v[20:21], v[20:21]
	v_add_f32_e32 v6, v6, v7
	v_add_f32_e32 v6, v6, v8
	v_pk_mul_f32 v[26:27], v[24:25], v[24:25]
	v_add_f32_e32 v6, v6, v9
	v_add_f32_e32 v6, v6, v26
	v_pk_mul_f32 v[28:29], v[22:23], v[22:23]
	v_add_f32_e32 v6, v6, v27
	v_add_f32_e32 v6, v6, v28
	v_add_f32_e32 v6, v6, v29
	s_nop 1
	v_add_f32_dpp v6, v6, v6 quad_perm:[1,0,3,2] row_mask:0xf bank_mask:0xf bound_ctrl:1
	s_nop 1
	v_add_f32_dpp v6, v6, v6 quad_perm:[2,3,0,1] row_mask:0xf bank_mask:0xf bound_ctrl:1
	s_nop 1
	v_add_f32_dpp v6, v6, v6 row_half_mirror row_mask:0xf bank_mask:0xf bound_ctrl:1
	s_nop 1
	v_add_f32_dpp v6, v6, v6 row_mirror row_mask:0xf bank_mask:0xf bound_ctrl:1
	s_nop 0
	v_readlane_b32 s8, v6, 16
	v_readlane_b32 s9, v6, 48
	v_readlane_b32 s0, v6, 0
	v_readlane_b32 s1, v6, 32
	v_mov_b32_e32 v6, s8
	v_mov_b32_e32 v7, s9
	v_pk_add_f32 v[6:7], s[0:1], v[6:7]
	s_nop 0
	v_add_f32_e32 v6, v6, v7
	v_fmac_f32_e32 v59, 0x3b000000, v6
	v_mul_f32_e32 v6, 0x4f800000, v59
	v_cmp_gt_f32_e32 vcc, s12, v59
	s_nop 1
	v_cndmask_b32_e32 v6, v59, v6, vcc
	v_sqrt_f32_e32 v7, v6
	s_nop 0
	v_add_u32_e32 v8, -1, v7
	v_add_u32_e32 v9, 1, v7
	v_fma_f32 v26, -v8, v7, v6
	v_fma_f32 v27, -v9, v7, v6
	v_cmp_ge_f32_e64 s[0:1], 0, v26
	s_nop 1
	v_cndmask_b32_e64 v7, v7, v8, s[0:1]
	v_cmp_lt_f32_e64 s[0:1], 0, v27
	v_lshl_add_u64 v[26:27], v[4:5], 0, v[0:1]
	s_nop 0
	v_cndmask_b32_e64 v7, v7, v9, s[0:1]
	v_mul_f32_e32 v8, 0x37800000, v7
	v_cndmask_b32_e32 v7, v7, v8, vcc
	v_cmp_class_f32_e32 vcc, v6, v60
	s_nop 1
	v_cndmask_b32_e32 v6, v7, v6, vcc
	v_div_scale_f32 v7, s[0:1], v6, v6, 1.0
	v_rcp_f32_e32 v8, v7
	s_mov_b32 s0, 0x43000000
	v_fma_f32 v0, -v7, v8, 1.0
	v_fmac_f32_e32 v8, v0, v8
	v_div_scale_f32 v0, vcc, 1.0, v6, 1.0
	v_mul_f32_e32 v4, v0, v8
	v_fma_f32 v5, -v7, v4, v0
	v_fmac_f32_e32 v4, v5, v8
	v_fma_f32 v0, -v7, v4, v0
	v_div_fmas_f32 v0, v0, v8, v4
	v_div_fixup_f32 v0, v0, v6, 1.0
	v_pk_mul_f32 v[4:5], v[44:45], v[18:19]
	v_pk_mul_f32 v[6:7], v[46:47], v[20:21]
	v_pk_fma_f32 v[4:5], v[0:1], v[4:5], v[48:49] op_sel_hi:[0,1,1]
	v_pk_mul_f32 v[8:9], v[10:11], v[24:25]
	v_pk_fma_f32 v[6:7], v[0:1], v[6:7], v[50:51] op_sel_hi:[0,1,1]
	v_pk_fma_f32 v[8:9], v[0:1], v[8:9], v[14:15] op_sel_hi:[0,1,1]
	v_pk_mul_f32 v[10:11], v[12:13], v[22:23]
	v_fma_mixlo_f16 v12, v4, s0, 0
	v_pk_fma_f32 v[10:11], v[0:1], v[10:11], v[16:17] op_sel_hi:[0,1,1]
	global_store_dwordx4 v[26:27], v[4:7], off sc1
	global_store_dwordx4 v[26:27], v[8:11], off offset:1024 sc1
	v_mul_f32_e32 v0, 0x43000000, v4
	v_fma_mixlo_f16 v4, v4, s0, -v12 op_sel_hi:[0,0,1]
	v_fma_mixlo_f16 v12, v8, s0, 0
	v_mul_f32_e32 v13, 0x43000000, v8
	v_fma_mixlo_f16 v8, v8, s0, -v12 op_sel_hi:[0,0,1]
	v_mul_f32_e32 v12, 0x43000000, v5
	v_fma_mixlo_f16 v14, v5, s0, 0
	v_cvt_pk_f16_f32 v12, v0, v12
	v_mul_f32_e32 v0, 0x43000000, v9
	v_pk_mul_f32 v[16:17], v[6:7], s[0:1] op_sel_hi:[1,0]
	v_fma_mixhi_f16 v4, v5, s0, -v14 op_sel_hi:[0,0,1]
	v_cvt_pk_f16_f32 v14, v13, v0
	v_cvt_pk_f16_f32 v13, v16, v17
	v_pk_mul_f32 v[18:19], v[10:11], s[0:1] op_sel_hi:[1,0]
	v_cvt_f32_f16_e32 v16, v13
	v_cvt_f32_f16_sdwa v17, v13 dst_sel:DWORD dst_unused:UNUSED_PAD src0_sel:WORD_1
	v_cvt_pk_f16_f32 v15, v18, v19
	v_cvt_f32_f16_e32 v18, v15
	v_cvt_f32_f16_sdwa v19, v15 dst_sel:DWORD dst_unused:UNUSED_PAD src0_sel:WORD_1
	v_fma_mixlo_f16 v5, v9, s0, 0
	v_pk_fma_f32 v[6:7], v[6:7], s[0:1], v[16:17] op_sel_hi:[1,0,1] neg_lo:[0,0,1] neg_hi:[0,0,1]
	v_fma_mixhi_f16 v8, v9, s0, -v5 op_sel_hi:[0,0,1]
	v_cvt_pk_f16_f32 v5, v6, v7
	v_pk_fma_f32 v[6:7], v[10:11], s[0:1], v[18:19] op_sel_hi:[1,0,1] neg_lo:[0,0,1] neg_hi:[0,0,1]
	v_lshlrev_b32_e32 v0, 1, v58
	v_cvt_pk_f16_f32 v9, v6, v7
	v_lshl_add_u64 v[6:7], s[6:7], 0, v[2:3]
	v_lshl_add_u64 v[2:3], s[2:3], 0, v[2:3]
	v_lshl_add_u64 v[6:7], v[6:7], 0, v[0:1]
	v_lshl_add_u64 v[0:1], v[2:3], 0, v[0:1]
	global_store_dwordx2 v[6:7], v[12:13], off sc1
	global_store_dwordx2 v[6:7], v[14:15], off offset:512 sc1
	global_store_dwordx2 v[0:1], v[4:5], off sc1
	global_store_dwordx2 v[0:1], v[8:9], off offset:512 sc1
	s_endpgm
	s_endpgm
	s_endpgm
	s_endpgm
	s_endpgm
	s_endpgm
	s_endpgm
	s_endpgm
	s_endpgm
	s_endpgm
	s_endpgm
	s_endpgm
	s_endpgm
	s_endpgm
	s_endpgm
	s_endpgm
	s_endpgm
	s_endpgm
	s_endpgm
	s_endpgm
	s_endpgm
	s_endpgm
	s_endpgm
	s_endpgm
	s_endpgm
	s_endpgm
	s_endpgm
	s_endpgm
	s_endpgm
	s_endpgm
	s_endpgm
	s_endpgm
	s_endpgm
	s_endpgm
	s_endpgm
	s_endpgm
	s_endpgm
	s_endpgm
	s_endpgm
	s_endpgm
	s_endpgm
	s_endpgm
	s_endpgm
	s_endpgm
	s_endpgm
	s_endpgm

.LBB13_5:
	v_lshlrev_b32_e32 v0, 2, v0
	v_and_b32_e32 v58, 0xfc, v0
	v_lshlrev_b64 v[4:5], 11, v[4:5]
	s_load_dwordx2 s[0:1], s[0:1], 0x8
	v_lshlrev_b32_e32 v0, 2, v58
	v_mov_b32_e32 v1, 0
	s_waitcnt lgkmcnt(0)
	v_lshl_add_u64 v[4:5], s[24:25], 0, v[4:5]
	v_lshl_add_u64 v[4:5], v[4:5], 0, v[0:1]
	global_load_dwordx4 v[8:11], v[4:5], off
	global_load_dwordx4 v[12:15], v0, s[20:21]
	global_load_dwordx4 v[16:19], v0, s[20:21] offset:1024
	global_load_dwordx4 v[20:23], v[4:5], off offset:1024
	v_lshlrev_b64 v[4:5], 11, v[2:3]
	v_lshl_add_u64 v[32:33], s[22:23], 0, v[4:5]
	v_lshl_add_u64 v[34:35], v[32:33], 0, v[0:1]
	v_lshl_add_u64 v[32:33], s[0:1], 2, v[32:33]
	global_load_dwordx4 v[24:27], v[34:35], off
	global_load_dwordx4 v[28:31], v[34:35], off offset:1024
	v_lshl_add_u64 v[40:41], v[32:33], 0, v[0:1]
	global_load_dwordx4 v[32:35], v[40:41], off
	global_load_dwordx4 v[36:39], v[40:41], off offset:1024
	global_load_dwordx4 v[44:47], v0, s[12:13] offset:1024
	v_lshlrev_b64 v[6:7], 11, v[6:7]
	global_load_dwordx4 v[40:43], v0, s[12:13]
	v_lshl_add_u64 v[6:7], s[18:19], 0, v[6:7]
	global_load_dwordx4 v[48:51], v0, s[14:15]
	v_lshl_add_u64 v[52:53], v[6:7], 0, v[0:1]
	v_mov_b32_e32 v59, 0x3727c5ac
	s_mov_b32 s12, 0xf800000
	v_mov_b32_e32 v60, 0x260
	v_lshl_add_u64 v[4:5], s[4:5], 0, v[4:5]
	v_lshlrev_b64 v[2:3], 10, v[2:3]
	s_waitcnt vmcnt(9)
	v_pk_add_f32 v[54:55], v[12:13], v[8:9]
	v_pk_add_f32 v[56:57], v[14:15], v[10:11]
	s_waitcnt vmcnt(7)
	v_pk_add_f32 v[20:21], v[16:17], v[20:21]
	v_pk_add_f32 v[18:19], v[18:19], v[22:23]
	global_load_dwordx4 v[6:9], v0, s[8:9]
	global_load_dwordx4 v[10:13], v0, s[10:11]
	global_load_dwordx4 v[14:17], v0, s[14:15] offset:1024
	s_waitcnt vmcnt(9)
	v_pk_add_f32 v[54:55], v[54:55], v[24:25]
	v_pk_add_f32 v[26:27], v[56:57], v[26:27]
	s_waitcnt vmcnt(8)
	v_pk_add_f32 v[28:29], v[20:21], v[28:29]
	v_pk_add_f32 v[30:31], v[18:19], v[30:31]
	global_load_dwordx4 v[18:21], v0, s[8:9] offset:1024
	global_load_dwordx4 v[22:25], v0, s[10:11] offset:1024
	s_waitcnt vmcnt(9)
	v_pk_add_f32 v[54:55], v[54:55], v[32:33]
	v_pk_add_f32 v[34:35], v[26:27], v[34:35]
	s_waitcnt vmcnt(8)
	v_pk_add_f32 v[36:37], v[28:29], v[36:37]
	v_pk_add_f32 v[38:39], v[30:31], v[38:39]
	global_load_dwordx4 v[26:29], v[52:53], off
	global_load_dwordx4 v[30:33], v[52:53], off offset:1024
	v_add_f32_e32 v52, 0, v54
	v_add_f32_e32 v52, v52, v55
	v_add_f32_e32 v52, v52, v34
	v_add_f32_e32 v52, v52, v35
	v_add_f32_e32 v52, v52, v36
	v_add_f32_e32 v52, v52, v37
	v_add_f32_e32 v52, v52, v38
	v_add_f32_e32 v52, v52, v39
	s_nop 1
	v_add_f32_dpp v52, v52, v52 quad_perm:[1,0,3,2] row_mask:0xf bank_mask:0xf bound_ctrl:1
	s_nop 1
	v_add_f32_dpp v52, v52, v52 quad_perm:[2,3,0,1] row_mask:0xf bank_mask:0xf bound_ctrl:1
	s_nop 1
	v_add_f32_dpp v52, v52, v52 row_half_mirror row_mask:0xf bank_mask:0xf bound_ctrl:1
	s_nop 1
	v_add_f32_dpp v52, v52, v52 row_mirror row_mask:0xf bank_mask:0xf bound_ctrl:1
	s_nop 0
	v_readlane_b32 s8, v52, 16
	v_readlane_b32 s9, v52, 48
	v_readlane_b32 s0, v52, 0
	v_readlane_b32 s1, v52, 32
	v_mov_b32_e32 v52, s8
	v_mov_b32_e32 v53, s9
	v_pk_add_f32 v[52:53], s[0:1], v[52:53]
	s_nop 0
	v_add_f32_e32 v52, v52, v53
	v_mul_f32_e32 v52, 0x3b000000, v52
	v_pk_add_f32 v[54:55], v[54:55], v[52:53] op_sel_hi:[1,0] neg_lo:[0,1] neg_hi:[0,1]
	v_pk_add_f32 v[34:35], v[34:35], v[52:53] op_sel_hi:[1,0] neg_lo:[0,1] neg_hi:[0,1]
	v_pk_add_f32 v[36:37], v[36:37], v[52:53] op_sel_hi:[1,0] neg_lo:[0,1] neg_hi:[0,1]
	v_pk_add_f32 v[38:39], v[38:39], v[52:53] op_sel_hi:[1,0] neg_lo:[0,1] neg_hi:[0,1]
	v_pk_mul_f32 v[52:53], v[54:55], v[54:55]
	s_waitcnt vmcnt(8)
	v_pk_mul_f32 v[40:41], v[40:41], v[54:55]
	v_add_f32_e32 v56, v52, v53
	v_pk_mul_f32 v[52:53], v[34:35], v[34:35]
	v_pk_mul_f32 v[34:35], v[42:43], v[34:35]
	v_add_f32_e32 v52, v56, v52
	v_add_f32_e32 v56, v52, v53
	v_pk_mul_f32 v[52:53], v[36:37], v[36:37]
	v_pk_mul_f32 v[36:37], v[44:45], v[36:37]
	v_add_f32_e32 v52, v56, v52
	v_add_f32_e32 v56, v52, v53
	v_pk_mul_f32 v[52:53], v[38:39], v[38:39]
	v_pk_mul_f32 v[38:39], v[46:47], v[38:39]
	v_add_f32_e32 v52, v56, v52
	v_add_f32_e32 v52, v52, v53
	s_nop 1
	v_add_f32_dpp v52, v52, v52 quad_perm:[1,0,3,2] row_mask:0xf bank_mask:0xf bound_ctrl:1
	s_nop 1
	v_add_f32_dpp v52, v52, v52 quad_perm:[2,3,0,1] row_mask:0xf bank_mask:0xf bound_ctrl:1
	s_nop 1
	v_add_f32_dpp v52, v52, v52 row_half_mirror row_mask:0xf bank_mask:0xf bound_ctrl:1
	s_nop 1
	v_add_f32_dpp v52, v52, v52 row_mirror row_mask:0xf bank_mask:0xf bound_ctrl:1
	s_nop 0
	v_readlane_b32 s8, v52, 16
	v_readlane_b32 s9, v52, 48
	v_readlane_b32 s0, v52, 0
	v_readlane_b32 s1, v52, 32
	v_mov_b32_e32 v52, s8
	v_mov_b32_e32 v53, s9
	v_pk_add_f32 v[52:53], s[0:1], v[52:53]
	s_nop 0
	v_add_f32_e32 v52, v52, v53
	v_fmamk_f32 v52, v52, 0x3b000000, v59
	v_mul_f32_e32 v53, 0x4f800000, v52
	v_cmp_gt_f32_e32 vcc, s12, v52
	s_nop 1
	v_cndmask_b32_e32 v52, v52, v53, vcc
	v_sqrt_f32_e32 v53, v52
	s_nop 0
	v_add_u32_e32 v42, -1, v53
	v_add_u32_e32 v43, 1, v53
	v_fma_f32 v44, -v42, v53, v52
	v_fma_f32 v45, -v43, v53, v52
	v_cmp_ge_f32_e64 s[0:1], 0, v44
	s_nop 1
	v_cndmask_b32_e64 v42, v53, v42, s[0:1]
	v_cmp_lt_f32_e64 s[0:1], 0, v45
	s_nop 1
	v_cndmask_b32_e64 v42, v42, v43, s[0:1]
	v_mul_f32_e32 v43, 0x37800000, v42
	v_cndmask_b32_e32 v42, v42, v43, vcc
	v_cmp_class_f32_e32 vcc, v52, v60
	s_nop 1
	v_cndmask_b32_e32 v42, v42, v52, vcc
	v_div_scale_f32 v43, s[0:1], v42, v42, 1.0
	v_rcp_f32_e32 v44, v43
	v_div_scale_f32 v45, vcc, 1.0, v42, 1.0
	v_fma_f32 v46, -v43, v44, 1.0
	v_fmac_f32_e32 v44, v46, v44
	v_mul_f32_e32 v46, v45, v44
	v_fma_f32 v47, -v43, v46, v45
	v_fmac_f32_e32 v46, v47, v44
	v_fma_f32 v43, -v43, v46, v45
	v_div_fmas_f32 v43, v43, v44, v46
	v_div_fixup_f32 v42, v43, v42, 1.0
	s_waitcnt vmcnt(7)
	v_pk_fma_f32 v[40:41], v[42:43], v[40:41], v[48:49] op_sel_hi:[0,1,1]
	s_waitcnt vmcnt(4)
	v_pk_fma_f32 v[14:15], v[42:43], v[36:37], v[14:15] op_sel_hi:[0,1,1]
	s_waitcnt vmcnt(1)
	v_pk_add_f32 v[26:27], v[40:41], v[26:27]
	v_pk_fma_f32 v[34:35], v[42:43], v[34:35], v[50:51] op_sel_hi:[0,1,1]
	s_waitcnt vmcnt(0)
	v_pk_add_f32 v[14:15], v[14:15], v[30:31]
	v_add_f32_e32 v30, 0, v26
	v_pk_add_f32 v[28:29], v[34:35], v[28:29]
	v_add_f32_e32 v30, v30, v27
	v_add_f32_e32 v30, v30, v28
	v_add_f32_e32 v30, v30, v29
	v_pk_fma_f32 v[16:17], v[42:43], v[38:39], v[16:17] op_sel_hi:[0,1,1]
	v_add_f32_e32 v30, v30, v14
	v_pk_add_f32 v[16:17], v[16:17], v[32:33]
	v_add_f32_e32 v30, v30, v15
	v_add_f32_e32 v30, v30, v16
	v_add_f32_e32 v30, v30, v17
	s_nop 1
	v_add_f32_dpp v30, v30, v30 quad_perm:[1,0,3,2] row_mask:0xf bank_mask:0xf bound_ctrl:1
	s_nop 1
	v_add_f32_dpp v30, v30, v30 quad_perm:[2,3,0,1] row_mask:0xf bank_mask:0xf bound_ctrl:1
	s_nop 1
	v_add_f32_dpp v30, v30, v30 row_half_mirror row_mask:0xf bank_mask:0xf bound_ctrl:1
	s_nop 1
	v_add_f32_dpp v30, v30, v30 row_mirror row_mask:0xf bank_mask:0xf bound_ctrl:1
	s_nop 0
	v_readlane_b32 s8, v30, 16
	v_readlane_b32 s9, v30, 48
	v_readlane_b32 s0, v30, 0
	v_readlane_b32 s1, v30, 32
	v_mov_b32_e32 v30, s8
	v_mov_b32_e32 v31, s9
	v_pk_add_f32 v[30:31], s[0:1], v[30:31]
	s_nop 0
	v_add_f32_e32 v30, v30, v31
	v_mul_f32_e32 v30, 0x3b000000, v30
	v_pk_add_f32 v[26:27], v[26:27], v[30:31] op_sel_hi:[1,0] neg_lo:[0,1] neg_hi:[0,1]
	v_pk_add_f32 v[28:29], v[28:29], v[30:31] op_sel_hi:[1,0] neg_lo:[0,1] neg_hi:[0,1]
	v_pk_add_f32 v[14:15], v[14:15], v[30:31] op_sel_hi:[1,0] neg_lo:[0,1] neg_hi:[0,1]
	v_pk_add_f32 v[16:17], v[16:17], v[30:31] op_sel_hi:[1,0] neg_lo:[0,1] neg_hi:[0,1]
	v_pk_mul_f32 v[30:31], v[26:27], v[26:27]
	v_pk_mul_f32 v[32:33], v[28:29], v[28:29]
	v_add_f32_e32 v30, v30, v31
	v_add_f32_e32 v30, v30, v32
	v_pk_mul_f32 v[34:35], v[14:15], v[14:15]
	v_add_f32_e32 v30, v30, v33
	v_add_f32_e32 v30, v30, v34
	v_pk_mul_f32 v[36:37], v[16:17], v[16:17]
	v_add_f32_e32 v30, v30, v35
	v_add_f32_e32 v30, v30, v36
	v_add_f32_e32 v30, v30, v37
	s_nop 1
	v_add_f32_dpp v30, v30, v30 quad_perm:[1,0,3,2] row_mask:0xf bank_mask:0xf bound_ctrl:1
	s_nop 1
	v_add_f32_dpp v30, v30, v30 quad_perm:[2,3,0,1] row_mask:0xf bank_mask:0xf bound_ctrl:1
	s_nop 1
	v_add_f32_dpp v30, v30, v30 row_half_mirror row_mask:0xf bank_mask:0xf bound_ctrl:1
	s_nop 1
	v_add_f32_dpp v30, v30, v30 row_mirror row_mask:0xf bank_mask:0xf bound_ctrl:1
	s_nop 0
	v_readlane_b32 s8, v30, 16
	v_readlane_b32 s9, v30, 48
	v_readlane_b32 s0, v30, 0
	v_readlane_b32 s1, v30, 32
	v_mov_b32_e32 v30, s8
	v_mov_b32_e32 v31, s9
	v_pk_add_f32 v[30:31], s[0:1], v[30:31]
	s_nop 0
	v_add_f32_e32 v30, v30, v31
	v_fmac_f32_e32 v59, 0x3b000000, v30
	v_mul_f32_e32 v30, 0x4f800000, v59
	v_cmp_gt_f32_e32 vcc, s12, v59
	s_nop 1
	v_cndmask_b32_e32 v30, v59, v30, vcc
	v_sqrt_f32_e32 v31, v30
	s_nop 0
	v_add_u32_e32 v32, -1, v31
	v_fma_f32 v33, -v32, v31, v30
	v_cmp_ge_f32_e64 s[0:1], 0, v33
	v_add_u32_e32 v33, 1, v31
	s_nop 0
	v_cndmask_b32_e64 v32, v31, v32, s[0:1]
	v_fma_f32 v31, -v33, v31, v30
	v_cmp_lt_f32_e64 s[0:1], 0, v31
	s_nop 1
	v_cndmask_b32_e64 v31, v32, v33, s[0:1]
	v_mul_f32_e32 v32, 0x37800000, v31
	v_cndmask_b32_e32 v31, v31, v32, vcc
	v_cmp_class_f32_e32 vcc, v30, v60
	s_nop 1
	v_cndmask_b32_e32 v32, v31, v30, vcc
	v_div_scale_f32 v33, s[0:1], v32, v32, 1.0
	v_rcp_f32_e32 v34, v33
	v_lshl_add_u64 v[30:31], v[4:5], 0, v[0:1]
	s_mov_b32 s0, 0x43000000
	v_fma_f32 v0, -v33, v34, 1.0
	v_fmac_f32_e32 v34, v0, v34
	v_div_scale_f32 v0, vcc, 1.0, v32, 1.0
	v_mul_f32_e32 v4, v0, v34
	v_fma_f32 v5, -v33, v4, v0
	v_fmac_f32_e32 v4, v5, v34
	v_fma_f32 v0, -v33, v4, v0
	v_div_fmas_f32 v0, v0, v34, v4
	v_div_fixup_f32 v0, v0, v32, 1.0
	v_pk_mul_f32 v[4:5], v[6:7], v[26:27]
	v_pk_mul_f32 v[6:7], v[8:9], v[28:29]
	v_pk_fma_f32 v[4:5], v[0:1], v[4:5], v[10:11] op_sel_hi:[0,1,1]
	v_pk_mul_f32 v[8:9], v[18:19], v[14:15]
	v_pk_fma_f32 v[6:7], v[0:1], v[6:7], v[12:13] op_sel_hi:[0,1,1]
	v_pk_fma_f32 v[8:9], v[0:1], v[8:9], v[22:23] op_sel_hi:[0,1,1]
	v_pk_mul_f32 v[10:11], v[20:21], v[16:17]
	v_fma_mixlo_f16 v12, v4, s0, 0
	v_pk_fma_f32 v[10:11], v[0:1], v[10:11], v[24:25] op_sel_hi:[0,1,1]
	global_store_dwordx4 v[30:31], v[4:7], off sc1
	global_store_dwordx4 v[30:31], v[8:11], off offset:1024 sc1
	v_mul_f32_e32 v0, 0x43000000, v4
	v_fma_mixlo_f16 v4, v4, s0, -v12 op_sel_hi:[0,0,1]
	v_fma_mixlo_f16 v12, v8, s0, 0
	v_mul_f32_e32 v13, 0x43000000, v8
	v_fma_mixlo_f16 v8, v8, s0, -v12 op_sel_hi:[0,0,1]
	v_mul_f32_e32 v12, 0x43000000, v5
	v_fma_mixlo_f16 v14, v5, s0, 0
	v_cvt_pk_f16_f32 v12, v0, v12
	v_mul_f32_e32 v0, 0x43000000, v9
	v_pk_mul_f32 v[16:17], v[6:7], s[0:1] op_sel_hi:[1,0]
	v_fma_mixhi_f16 v4, v5, s0, -v14 op_sel_hi:[0,0,1]
	v_cvt_pk_f16_f32 v14, v13, v0
	v_cvt_pk_f16_f32 v13, v16, v17
	v_pk_mul_f32 v[18:19], v[10:11], s[0:1] op_sel_hi:[1,0]
	v_cvt_f32_f16_e32 v16, v13
	v_cvt_f32_f16_sdwa v17, v13 dst_sel:DWORD dst_unused:UNUSED_PAD src0_sel:WORD_1
	v_cvt_pk_f16_f32 v15, v18, v19
	v_cvt_f32_f16_e32 v18, v15
	v_cvt_f32_f16_sdwa v19, v15 dst_sel:DWORD dst_unused:UNUSED_PAD src0_sel:WORD_1
	v_fma_mixlo_f16 v5, v9, s0, 0
	v_pk_fma_f32 v[6:7], v[6:7], s[0:1], v[16:17] op_sel_hi:[1,0,1] neg_lo:[0,0,1] neg_hi:[0,0,1]
	v_fma_mixhi_f16 v8, v9, s0, -v5 op_sel_hi:[0,0,1]
	v_cvt_pk_f16_f32 v5, v6, v7
	v_pk_fma_f32 v[6:7], v[10:11], s[0:1], v[18:19] op_sel_hi:[1,0,1] neg_lo:[0,0,1] neg_hi:[0,0,1]
	v_lshlrev_b32_e32 v0, 1, v58
	v_cvt_pk_f16_f32 v9, v6, v7
	v_lshl_add_u64 v[6:7], s[6:7], 0, v[2:3]
	v_lshl_add_u64 v[2:3], s[2:3], 0, v[2:3]
	v_lshl_add_u64 v[6:7], v[6:7], 0, v[0:1]
	v_lshl_add_u64 v[0:1], v[2:3], 0, v[0:1]
	global_store_dwordx2 v[6:7], v[12:13], off sc1
	global_store_dwordx2 v[6:7], v[14:15], off offset:512 sc1
	global_store_dwordx2 v[0:1], v[4:5], off sc1
	global_store_dwordx2 v[0:1], v[8:9], off offset:512 sc1
	s_endpgm
	s_endpgm
	s_endpgm
	s_endpgm
	s_endpgm
	s_endpgm
	s_endpgm
	s_endpgm
	s_endpgm
	s_endpgm
	s_endpgm
	s_endpgm
	s_endpgm
	s_endpgm
	s_endpgm
	s_endpgm
	s_endpgm
	s_endpgm
	s_endpgm
	s_endpgm
	s_endpgm
	s_endpgm
	s_endpgm
	s_endpgm
	s_endpgm
	s_endpgm
	s_endpgm

.LBB14_5:
	v_lshlrev_b32_e32 v0, 2, v0
	v_and_b32_e32 v60, 0xfc, v0
	v_lshlrev_b64 v[8:9], 11, v[8:9]
	v_lshlrev_b32_e32 v0, 2, v60
	v_mov_b32_e32 v1, 0
	s_waitcnt lgkmcnt(0)
	v_lshl_add_u64 v[8:9], s[24:25], 0, v[8:9]
	v_lshl_add_u64 v[24:25], v[8:9], 0, v[0:1]
	global_load_dwordx4 v[8:11], v[24:25], off
	global_load_dwordx4 v[12:15], v0, s[20:21]
	global_load_dwordx4 v[16:19], v0, s[20:21] offset:1024
	global_load_dwordx4 v[20:23], v[24:25], off offset:1024
	s_load_dwordx2 s[0:1], s[0:1], 0x8
	v_lshlrev_b64 v[4:5], 11, v[2:3]
	v_lshl_add_u64 v[36:37], s[22:23], 0, v[4:5]
	v_lshl_add_u64 v[28:29], v[36:37], 0, v[0:1]
	global_load_dwordx4 v[24:27], v[28:29], off
	s_waitcnt lgkmcnt(0)
	v_lshl_add_u64 v[30:31], s[0:1], 2, v[36:37]
	v_lshl_add_u64 v[38:39], v[30:31], 0, v[0:1]
	v_lshl_add_u64 v[32:33], s[0:1], 3, v[36:37]
	v_lshl_add_u64 v[44:45], v[32:33], 0, v[0:1]
	global_load_dwordx4 v[32:35], v[38:39], off
	v_mad_u64_u32 v[48:49], s[16:17], s0, 12, v[36:37]
	global_load_dwordx4 v[28:31], v[28:29], off offset:1024
	v_mov_b32_e32 v40, v49
	v_mad_u64_u32 v[46:47], s[0:1], s1, 12, v[40:41]
	global_load_dwordx4 v[40:43], v[44:45], off
	v_mov_b32_e32 v49, v46
	v_lshl_add_u64 v[56:57], v[48:49], 0, v[0:1]
	global_load_dwordx4 v[36:39], v[38:39], off offset:1024
	v_lshlrev_b64 v[6:7], 11, v[6:7]
	global_load_dwordx4 v[44:47], v[44:45], off offset:1024
	s_nop 0
	global_load_dwordx4 v[48:51], v[56:57], off
	global_load_dwordx4 v[52:55], v[56:57], off offset:1024
	v_lshl_add_u64 v[6:7], s[18:19], 0, v[6:7]
	v_lshl_add_u64 v[56:57], v[6:7], 0, v[0:1]
	v_mov_b32_e32 v61, 0x3727c5ac
	s_mov_b32 s16, 0xf800000
	v_lshl_add_u64 v[4:5], s[4:5], 0, v[4:5]
	v_lshlrev_b64 v[2:3], 10, v[2:3]
	s_waitcnt vmcnt(10)
	v_pk_add_f32 v[58:59], v[12:13], v[8:9]
	v_pk_add_f32 v[14:15], v[14:15], v[10:11]
	global_load_dwordx4 v[6:9], v0, s[12:13]
	global_load_dwordx4 v[10:13], v0, s[14:15]
	s_waitcnt vmcnt(10)
	v_pk_add_f32 v[16:17], v[16:17], v[20:21]
	v_pk_add_f32 v[18:19], v[18:19], v[22:23]
	s_waitcnt vmcnt(9)
	v_pk_add_f32 v[22:23], v[58:59], v[24:25]
	v_pk_add_f32 v[24:25], v[14:15], v[26:27]
	s_waitcnt vmcnt(8)
	v_pk_add_f32 v[32:33], v[22:23], v[32:33]
	v_pk_add_f32 v[34:35], v[24:25], v[34:35]
	s_waitcnt vmcnt(7)
	v_pk_add_f32 v[58:59], v[16:17], v[28:29]
	v_pk_add_f32 v[30:31], v[18:19], v[30:31]
	global_load_dwordx4 v[14:17], v0, s[12:13] offset:1024
	global_load_dwordx4 v[18:21], v0, s[14:15] offset:1024
	global_load_dwordx4 v[22:25], v[56:57], off
	global_load_dwordx4 v[26:29], v[56:57], off offset:1024
	s_waitcnt vmcnt(10)
	v_pk_add_f32 v[32:33], v[32:33], v[40:41]
	v_pk_add_f32 v[34:35], v[34:35], v[42:43]
	s_waitcnt vmcnt(9)
	v_pk_add_f32 v[30:31], v[30:31], v[38:39]
	v_pk_add_f32 v[36:37], v[58:59], v[36:37]
	s_waitcnt vmcnt(7)
	v_pk_add_f32 v[32:33], v[32:33], v[48:49]
	v_pk_add_f32 v[34:35], v[34:35], v[50:51]
	v_add_f32_e32 v38, 0, v32
	v_add_f32_e32 v38, v38, v33
	v_pk_add_f32 v[36:37], v[36:37], v[44:45]
	v_add_f32_e32 v38, v38, v34
	s_waitcnt vmcnt(6)
	v_pk_add_f32 v[36:37], v[36:37], v[52:53]
	v_add_f32_e32 v38, v38, v35
	v_pk_add_f32 v[30:31], v[30:31], v[46:47]
	v_add_f32_e32 v38, v38, v36
	v_pk_add_f32 v[30:31], v[30:31], v[54:55]
	v_add_f32_e32 v38, v38, v37
	v_add_f32_e32 v38, v38, v30
	v_add_f32_e32 v38, v38, v31
	v_mov_b32_e32 v55, 0x260
	s_nop 0
	v_add_f32_dpp v38, v38, v38 quad_perm:[1,0,3,2] row_mask:0xf bank_mask:0xf bound_ctrl:1
	s_nop 1
	v_add_f32_dpp v38, v38, v38 quad_perm:[2,3,0,1] row_mask:0xf bank_mask:0xf bound_ctrl:1
	s_nop 1
	v_add_f32_dpp v38, v38, v38 row_half_mirror row_mask:0xf bank_mask:0xf bound_ctrl:1
	s_nop 1
	v_add_f32_dpp v38, v38, v38 row_mirror row_mask:0xf bank_mask:0xf bound_ctrl:1
	s_nop 0
	v_readlane_b32 s12, v38, 16
	v_readlane_b32 s13, v38, 48
	v_readlane_b32 s0, v38, 0
	v_readlane_b32 s1, v38, 32
	v_mov_b32_e32 v38, s12
	v_mov_b32_e32 v39, s13
	v_pk_add_f32 v[38:39], s[0:1], v[38:39]
	s_nop 0
	v_add_f32_e32 v38, v38, v39
	v_mul_f32_e32 v38, 0x3b000000, v38
	v_pk_add_f32 v[46:47], v[32:33], v[38:39] op_sel_hi:[1,0] neg_lo:[0,1] neg_hi:[0,1]
	v_pk_add_f32 v[48:49], v[34:35], v[38:39] op_sel_hi:[1,0] neg_lo:[0,1] neg_hi:[0,1]
	v_pk_add_f32 v[52:53], v[30:31], v[38:39] op_sel_hi:[1,0] neg_lo:[0,1] neg_hi:[0,1]
	v_pk_mul_f32 v[30:31], v[46:47], v[46:47]
	v_pk_mul_f32 v[32:33], v[48:49], v[48:49]
	v_add_f32_e32 v30, v30, v31
	v_pk_add_f32 v[50:51], v[36:37], v[38:39] op_sel_hi:[1,0] neg_lo:[0,1] neg_hi:[0,1]
	v_add_f32_e32 v30, v30, v32
	v_pk_mul_f32 v[34:35], v[50:51], v[50:51]
	v_add_f32_e32 v30, v30, v33
	v_add_f32_e32 v30, v30, v34
	v_pk_mul_f32 v[36:37], v[52:53], v[52:53]
	v_add_f32_e32 v30, v30, v35
	v_add_f32_e32 v30, v30, v36
	v_add_f32_e32 v30, v30, v37
	s_waitcnt vmcnt(5)
	v_pk_mul_f32 v[6:7], v[6:7], v[46:47]
	v_add_f32_dpp v30, v30, v30 quad_perm:[1,0,3,2] row_mask:0xf bank_mask:0xf bound_ctrl:1
	v_pk_mul_f32 v[8:9], v[8:9], v[48:49]
	s_nop 0
	v_add_f32_dpp v30, v30, v30 quad_perm:[2,3,0,1] row_mask:0xf bank_mask:0xf bound_ctrl:1
	s_nop 1
	v_add_f32_dpp v30, v30, v30 row_half_mirror row_mask:0xf bank_mask:0xf bound_ctrl:1
	s_nop 1
	v_add_f32_dpp v30, v30, v30 row_mirror row_mask:0xf bank_mask:0xf bound_ctrl:1
	s_nop 0
	v_readlane_b32 s12, v30, 16
	v_readlane_b32 s13, v30, 48
	v_readlane_b32 s0, v30, 0
	v_readlane_b32 s1, v30, 32
	v_mov_b32_e32 v30, s12
	v_mov_b32_e32 v31, s13
	v_pk_add_f32 v[30:31], s[0:1], v[30:31]
	s_nop 0
	v_add_f32_e32 v30, v30, v31
	v_fmamk_f32 v30, v30, 0x3b000000, v61
	v_mul_f32_e32 v31, 0x4f800000, v30
	v_cmp_gt_f32_e32 vcc, s16, v30
	s_nop 1
	v_cndmask_b32_e32 v54, v30, v31, vcc
	v_sqrt_f32_e32 v38, v54
	global_load_dwordx4 v[30:33], v0, s[8:9]
	global_load_dwordx4 v[34:37], v0, s[10:11]
	v_add_u32_e32 v39, -1, v38
	v_add_u32_e32 v56, 1, v38
	v_fma_f32 v40, -v39, v38, v54
	v_fma_f32 v41, -v56, v38, v54
	v_cmp_ge_f32_e64 s[0:1], 0, v40
	s_nop 1
	v_cndmask_b32_e64 v57, v38, v39, s[0:1]
	v_cmp_lt_f32_e64 s[0:1], 0, v41
	global_load_dwordx4 v[38:41], v0, s[8:9] offset:1024
	global_load_dwordx4 v[42:45], v0, s[10:11] offset:1024
	v_cndmask_b32_e64 v46, v57, v56, s[0:1]
	v_mul_f32_e32 v47, 0x37800000, v46
	v_cndmask_b32_e32 v46, v46, v47, vcc
	v_cmp_class_f32_e32 vcc, v54, v55
	s_nop 1
	v_cndmask_b32_e32 v46, v46, v54, vcc
	v_div_scale_f32 v47, s[0:1], v46, v46, 1.0
	v_rcp_f32_e32 v54, v47
	v_div_scale_f32 v48, vcc, 1.0, v46, 1.0
	v_fma_f32 v49, -v47, v54, 1.0
	v_fmac_f32_e32 v54, v49, v54
	v_mul_f32_e32 v49, v48, v54
	v_fma_f32 v56, -v47, v49, v48
	v_fmac_f32_e32 v49, v56, v54
	v_fma_f32 v47, -v47, v49, v48
	v_div_fmas_f32 v47, v47, v54, v49
	v_div_fixup_f32 v46, v47, v46, 1.0
	s_waitcnt vmcnt(8)
	v_pk_fma_f32 v[6:7], v[46:47], v[6:7], v[10:11] op_sel_hi:[0,1,1]
	s_waitcnt vmcnt(5)
	v_pk_add_f32 v[6:7], v[6:7], v[22:23]
	v_pk_fma_f32 v[8:9], v[46:47], v[8:9], v[12:13] op_sel_hi:[0,1,1]
	v_pk_mul_f32 v[10:11], v[14:15], v[50:51]
	v_add_f32_e32 v14, 0, v6
	v_add_f32_e32 v14, v14, v7
	v_pk_add_f32 v[8:9], v[8:9], v[24:25]
	v_pk_fma_f32 v[10:11], v[46:47], v[10:11], v[18:19] op_sel_hi:[0,1,1]
	v_add_f32_e32 v14, v14, v8
	v_pk_mul_f32 v[12:13], v[16:17], v[52:53]
	v_add_f32_e32 v14, v14, v9
	s_waitcnt vmcnt(4)
	v_pk_add_f32 v[10:11], v[10:11], v[26:27]
	v_pk_fma_f32 v[12:13], v[46:47], v[12:13], v[20:21] op_sel_hi:[0,1,1]
	v_add_f32_e32 v14, v14, v10
	v_add_f32_e32 v14, v14, v11
	v_pk_add_f32 v[12:13], v[12:13], v[28:29]
	s_nop 0
	v_add_f32_e32 v14, v14, v12
	v_add_f32_e32 v14, v14, v13
	s_nop 1
	v_add_f32_dpp v14, v14, v14 quad_perm:[1,0,3,2] row_mask:0xf bank_mask:0xf bound_ctrl:1
	s_nop 1
	v_add_f32_dpp v14, v14, v14 quad_perm:[2,3,0,1] row_mask:0xf bank_mask:0xf bound_ctrl:1
	s_nop 1
	v_add_f32_dpp v14, v14, v14 row_half_mirror row_mask:0xf bank_mask:0xf bound_ctrl:1
	s_nop 1
	v_add_f32_dpp v14, v14, v14 row_mirror row_mask:0xf bank_mask:0xf bound_ctrl:1
	s_nop 0
	v_readlane_b32 s8, v14, 16
	v_readlane_b32 s9, v14, 48
	v_readlane_b32 s0, v14, 0
	v_readlane_b32 s1, v14, 32
	v_mov_b32_e32 v14, s8
	v_mov_b32_e32 v15, s9
	v_pk_add_f32 v[14:15], s[0:1], v[14:15]
	s_nop 0
	v_add_f32_e32 v14, v14, v15
	v_mul_f32_e32 v14, 0x3b000000, v14
	v_pk_add_f32 v[6:7], v[6:7], v[14:15] op_sel_hi:[1,0] neg_lo:[0,1] neg_hi:[0,1]
	v_pk_add_f32 v[8:9], v[8:9], v[14:15] op_sel_hi:[1,0] neg_lo:[0,1] neg_hi:[0,1]
	v_pk_mul_f32 v[16:17], v[6:7], v[6:7]
	v_pk_mul_f32 v[18:19], v[8:9], v[8:9]
	v_add_f32_e32 v16, v16, v17
	v_pk_add_f32 v[10:11], v[10:11], v[14:15] op_sel_hi:[1,0] neg_lo:[0,1] neg_hi:[0,1]
	v_add_f32_e32 v16, v16, v18
	v_pk_mul_f32 v[20:21], v[10:11], v[10:11]
	v_add_f32_e32 v16, v16, v19
	v_pk_add_f32 v[12:13], v[12:13], v[14:15] op_sel_hi:[1,0] neg_lo:[0,1] neg_hi:[0,1]
	v_add_f32_e32 v16, v16, v20
	v_pk_mul_f32 v[14:15], v[12:13], v[12:13]
	v_add_f32_e32 v16, v16, v21
	v_add_f32_e32 v14, v16, v14
	v_add_f32_e32 v14, v14, v15
	s_nop 1
	v_add_f32_dpp v14, v14, v14 quad_perm:[1,0,3,2] row_mask:0xf bank_mask:0xf bound_ctrl:1
	s_nop 1
	v_add_f32_dpp v14, v14, v14 quad_perm:[2,3,0,1] row_mask:0xf bank_mask:0xf bound_ctrl:1
	s_nop 1
	v_add_f32_dpp v14, v14, v14 row_half_mirror row_mask:0xf bank_mask:0xf bound_ctrl:1
	s_nop 1
	v_add_f32_dpp v14, v14, v14 row_mirror row_mask:0xf bank_mask:0xf bound_ctrl:1
	s_nop 0
	v_readlane_b32 s8, v14, 16
	v_readlane_b32 s9, v14, 48
	v_readlane_b32 s0, v14, 0
	v_readlane_b32 s1, v14, 32
	v_mov_b32_e32 v14, s8
	v_mov_b32_e32 v15, s9
	v_pk_add_f32 v[14:15], s[0:1], v[14:15]
	s_nop 0
	v_add_f32_e32 v14, v14, v15
	v_fmac_f32_e32 v61, 0x3b000000, v14
	v_mul_f32_e32 v14, 0x4f800000, v61
	v_cmp_gt_f32_e32 vcc, s16, v61
	s_nop 1
	v_cndmask_b32_e32 v14, v61, v14, vcc
	v_sqrt_f32_e32 v15, v14
	s_nop 0
	v_add_u32_e32 v16, -1, v15
	v_fma_f32 v17, -v16, v15, v14
	v_cmp_ge_f32_e64 s[0:1], 0, v17
	v_add_u32_e32 v17, 1, v15
	s_nop 0
	v_cndmask_b32_e64 v16, v15, v16, s[0:1]
	v_fma_f32 v15, -v17, v15, v14
	v_cmp_lt_f32_e64 s[0:1], 0, v15
	s_nop 1
	v_cndmask_b32_e64 v15, v16, v17, s[0:1]
	v_mul_f32_e32 v16, 0x37800000, v15
	v_cndmask_b32_e32 v15, v15, v16, vcc
	v_cmp_class_f32_e32 vcc, v14, v55
	s_nop 1
	v_cndmask_b32_e32 v16, v15, v14, vcc
	v_div_scale_f32 v17, s[0:1], v16, v16, 1.0
	v_rcp_f32_e32 v18, v17
	v_lshl_add_u64 v[14:15], v[4:5], 0, v[0:1]
	s_mov_b32 s0, 0x43000000
	v_fma_f32 v0, -v17, v18, 1.0
	v_fmac_f32_e32 v18, v0, v18
	v_div_scale_f32 v0, vcc, 1.0, v16, 1.0
	v_mul_f32_e32 v4, v0, v18
	v_fma_f32 v5, -v17, v4, v0
	v_fmac_f32_e32 v4, v5, v18
	v_fma_f32 v0, -v17, v4, v0
	v_div_fmas_f32 v0, v0, v18, v4
	v_div_fixup_f32 v0, v0, v16, 1.0
	s_waitcnt vmcnt(3)
	v_pk_mul_f32 v[4:5], v[30:31], v[6:7]
	v_pk_mul_f32 v[6:7], v[32:33], v[8:9]
	s_waitcnt vmcnt(2)
	v_pk_fma_f32 v[4:5], v[0:1], v[4:5], v[34:35] op_sel_hi:[0,1,1]
	s_waitcnt vmcnt(1)
	v_pk_mul_f32 v[8:9], v[38:39], v[10:11]
	v_pk_fma_f32 v[6:7], v[0:1], v[6:7], v[36:37] op_sel_hi:[0,1,1]
	s_waitcnt vmcnt(0)
	v_pk_fma_f32 v[8:9], v[0:1], v[8:9], v[42:43] op_sel_hi:[0,1,1]
	v_pk_mul_f32 v[10:11], v[40:41], v[12:13]
	v_fma_mixlo_f16 v12, v4, s0, 0
	v_pk_fma_f32 v[10:11], v[0:1], v[10:11], v[44:45] op_sel_hi:[0,1,1]
	global_store_dwordx4 v[14:15], v[4:7], off sc1
	global_store_dwordx4 v[14:15], v[8:11], off offset:1024 sc1
	v_mul_f32_e32 v0, 0x43000000, v4
	v_fma_mixlo_f16 v4, v4, s0, -v12 op_sel_hi:[0,0,1]
	v_fma_mixlo_f16 v12, v8, s0, 0
	v_mul_f32_e32 v13, 0x43000000, v8
	v_fma_mixlo_f16 v8, v8, s0, -v12 op_sel_hi:[0,0,1]
	v_mul_f32_e32 v12, 0x43000000, v5
	v_fma_mixlo_f16 v14, v5, s0, 0
	v_cvt_pk_f16_f32 v12, v0, v12
	v_mul_f32_e32 v0, 0x43000000, v9
	v_pk_mul_f32 v[16:17], v[6:7], s[0:1] op_sel_hi:[1,0]
	v_fma_mixhi_f16 v4, v5, s0, -v14 op_sel_hi:[0,0,1]
	v_cvt_pk_f16_f32 v14, v13, v0
	v_cvt_pk_f16_f32 v13, v16, v17
	v_pk_mul_f32 v[18:19], v[10:11], s[0:1] op_sel_hi:[1,0]
	v_cvt_f32_f16_e32 v16, v13
	v_cvt_f32_f16_sdwa v17, v13 dst_sel:DWORD dst_unused:UNUSED_PAD src0_sel:WORD_1
	v_cvt_pk_f16_f32 v15, v18, v19
	v_cvt_f32_f16_e32 v18, v15
	v_cvt_f32_f16_sdwa v19, v15 dst_sel:DWORD dst_unused:UNUSED_PAD src0_sel:WORD_1
	v_fma_mixlo_f16 v5, v9, s0, 0
	v_pk_fma_f32 v[6:7], v[6:7], s[0:1], v[16:17] op_sel_hi:[1,0,1] neg_lo:[0,0,1] neg_hi:[0,0,1]
	v_fma_mixhi_f16 v8, v9, s0, -v5 op_sel_hi:[0,0,1]
	v_cvt_pk_f16_f32 v5, v6, v7
	v_pk_fma_f32 v[6:7], v[10:11], s[0:1], v[18:19] op_sel_hi:[1,0,1] neg_lo:[0,0,1] neg_hi:[0,0,1]
	v_lshlrev_b32_e32 v0, 1, v60
	v_cvt_pk_f16_f32 v9, v6, v7
	v_lshl_add_u64 v[6:7], s[6:7], 0, v[2:3]
	v_lshl_add_u64 v[2:3], s[2:3], 0, v[2:3]
	v_lshl_add_u64 v[6:7], v[6:7], 0, v[0:1]
	v_lshl_add_u64 v[0:1], v[2:3], 0, v[0:1]
	global_store_dwordx2 v[6:7], v[12:13], off sc1
	global_store_dwordx2 v[6:7], v[14:15], off offset:512 sc1
	global_store_dwordx2 v[0:1], v[4:5], off sc1
	global_store_dwordx2 v[0:1], v[8:9], off offset:512 sc1
	s_endpgm
	s_endpgm
	s_endpgm
	s_endpgm
	s_endpgm
	s_endpgm
	s_endpgm
	s_endpgm
	s_endpgm
	s_endpgm
	s_endpgm
	s_endpgm
	s_endpgm
	s_endpgm
	s_endpgm
	s_endpgm
	s_endpgm
	s_endpgm
	s_endpgm
	s_endpgm
	s_endpgm
	s_endpgm
	s_endpgm
	s_endpgm
	s_endpgm
	s_endpgm
	s_endpgm
	s_endpgm
	s_endpgm
	s_endpgm
	s_endpgm
	s_endpgm
	s_endpgm
	s_endpgm
	s_endpgm
	s_endpgm
	s_endpgm
	s_endpgm
	s_endpgm
	s_endpgm
	s_endpgm
	s_endpgm
	s_endpgm
	s_endpgm
	s_endpgm
	s_endpgm
	s_endpgm
	s_endpgm
	s_endpgm

.LBB15_5:
	v_lshlrev_b32_e32 v0, 2, v0
	v_and_b32_e32 v8, 0xfc, v0
	v_lshlrev_b64 v[4:5], 11, v[4:5]
	v_lshlrev_b32_e32 v0, 2, v8
	v_mov_b32_e32 v1, 0
	s_waitcnt lgkmcnt(0)
	v_lshl_add_u64 v[4:5], s[24:25], 0, v[4:5]
	v_lshl_add_u64 v[4:5], v[4:5], 0, v[0:1]
	global_load_dwordx4 v[10:13], v[4:5], off
	global_load_dwordx4 v[14:17], v0, s[20:21]
	global_load_dwordx4 v[18:21], v0, s[20:21] offset:1024
	global_load_dwordx4 v[22:25], v[4:5], off offset:1024
	s_load_dwordx2 s[0:1], s[0:1], 0x8
	v_lshlrev_b64 v[4:5], 11, v[2:3]
	v_lshl_add_u64 v[50:51], s[22:23], 0, v[4:5]
	v_lshl_add_u64 v[30:31], v[50:51], 0, v[0:1]
	global_load_dwordx4 v[26:29], v[30:31], off
	s_waitcnt lgkmcnt(0)
	v_lshl_add_u64 v[34:35], s[0:1], 2, v[50:51]
	global_load_dwordx4 v[30:33], v[30:31], off offset:1024
	v_lshl_add_u64 v[42:43], v[34:35], 0, v[0:1]
	global_load_dwordx4 v[34:37], v[42:43], off
	global_load_dwordx4 v[38:41], v[42:43], off offset:1024
	v_lshl_add_u64 v[42:43], s[0:1], 3, v[50:51]
	v_lshl_add_u64 v[52:53], v[42:43], 0, v[0:1]
	global_load_dwordx4 v[42:45], v[52:53], off
	global_load_dwordx4 v[46:49], v[52:53], off offset:1024
	v_mad_u64_u32 v[52:53], s[16:17], s0, 12, v[50:51]
	v_mad_u64_u32 v[56:57], s[16:17], s0, 20, v[50:51]
	v_mad_u64_u32 v[62:63], s[16:17], s0, 24, v[50:51]
	v_lshl_add_u64 v[54:55], s[0:1], 4, v[50:51]
	v_mad_u64_u32 v[50:51], s[16:17], s0, 28, v[50:51]
	v_lshl_add_u64 v[54:55], v[54:55], 0, v[0:1]
	v_lshlrev_b64 v[6:7], 11, v[6:7]
	v_lshl_add_u64 v[6:7], s[18:19], 0, v[6:7]
	v_lshl_add_u64 v[6:7], v[6:7], 0, v[0:1]
	v_lshl_add_u64 v[4:5], s[4:5], 0, v[4:5]
	v_lshlrev_b64 v[2:3], 10, v[2:3]
	s_waitcnt vmcnt(8)
	v_pk_add_f32 v[58:59], v[14:15], v[10:11]
	v_mov_b32_e32 v10, v53
	v_pk_add_f32 v[60:61], v[16:17], v[12:13]
	v_mov_b32_e32 v12, v57
	v_mad_u64_u32 v[10:11], s[16:17], s1, 12, v[10:11]
	v_mov_b32_e32 v53, v10
	v_mov_b32_e32 v10, v63
	v_mad_u64_u32 v[12:13], s[16:17], s1, 20, v[12:13]
	v_mov_b32_e32 v57, v12
	v_mov_b32_e32 v12, v51
	v_mad_u64_u32 v[10:11], s[16:17], s1, 24, v[10:11]
	s_waitcnt vmcnt(6)
	v_pk_add_f32 v[66:67], v[18:19], v[22:23]
	v_lshl_add_u64 v[22:23], v[52:53], 0, v[0:1]
	v_mad_u64_u32 v[64:65], s[0:1], s1, 28, v[12:13]
	v_mov_b32_e32 v63, v10
	v_pk_add_f32 v[68:69], v[20:21], v[24:25]
	global_load_dwordx4 v[10:13], v[54:55], off
	global_load_dwordx4 v[14:17], v[54:55], off offset:1024
	global_load_dwordx4 v[18:21], v[22:23], off
	v_lshl_add_u64 v[52:53], v[56:57], 0, v[0:1]
	s_waitcnt vmcnt(8)
	v_pk_add_f32 v[54:55], v[58:59], v[26:27]
	v_pk_add_f32 v[56:57], v[60:61], v[28:29]
	global_load_dwordx4 v[26:29], v[52:53], off
	v_lshl_add_u64 v[58:59], v[62:63], 0, v[0:1]
	global_load_dwordx4 v[22:25], v[22:23], off offset:1024
	v_mov_b32_e32 v51, v64
	s_waitcnt vmcnt(9)
	v_pk_add_f32 v[60:61], v[66:67], v[30:31]
	v_pk_add_f32 v[62:63], v[68:69], v[32:33]
	s_waitcnt vmcnt(8)
	v_pk_add_f32 v[54:55], v[54:55], v[34:35]
	v_pk_add_f32 v[56:57], v[56:57], v[36:37]
	global_load_dwordx4 v[30:33], v[52:53], off offset:1024
	global_load_dwordx4 v[34:37], v[58:59], off
	v_lshl_add_u64 v[50:51], v[50:51], 0, v[0:1]
	s_waitcnt vmcnt(9)
	v_pk_add_f32 v[52:53], v[60:61], v[38:39]
	v_pk_add_f32 v[60:61], v[62:63], v[40:41]
	s_waitcnt vmcnt(8)
	v_pk_add_f32 v[54:55], v[54:55], v[42:43]
	v_pk_add_f32 v[56:57], v[56:57], v[44:45]
	global_load_dwordx4 v[38:41], v[50:51], off
	global_load_dwordx4 v[42:45], v[58:59], off offset:1024
	s_waitcnt vmcnt(9)
	v_pk_add_f32 v[52:53], v[52:53], v[46:47]
	v_pk_add_f32 v[58:59], v[60:61], v[48:49]
	global_load_dwordx4 v[46:49], v[50:51], off offset:1024
	s_waitcnt vmcnt(7)
	v_pk_add_f32 v[18:19], v[54:55], v[18:19]
	s_nop 0
	v_pk_add_f32 v[10:11], v[18:19], v[10:11]
	v_pk_add_f32 v[20:21], v[56:57], v[20:21]
	v_mov_b32_e32 v57, 0x3727c5ac
	s_waitcnt vmcnt(6)
	v_pk_add_f32 v[18:19], v[10:11], v[26:27]
	v_pk_add_f32 v[12:13], v[20:21], v[12:13]
	s_waitcnt vmcnt(5)
	v_pk_add_f32 v[22:23], v[52:53], v[22:23]
	v_pk_add_f32 v[10:11], v[58:59], v[24:25]
	v_pk_add_f32 v[14:15], v[22:23], v[14:15]
	v_pk_add_f32 v[10:11], v[10:11], v[16:17]
	v_pk_add_f32 v[20:21], v[12:13], v[28:29]
	v_mov_b32_e32 v58, 0x260
	s_waitcnt vmcnt(4)
	v_pk_add_f32 v[50:51], v[14:15], v[30:31]
	v_pk_add_f32 v[52:53], v[10:11], v[32:33]
	global_load_dwordx4 v[10:13], v0, s[12:13]
	global_load_dwordx4 v[14:17], v0, s[14:15]
	s_waitcnt vmcnt(5)
	v_pk_add_f32 v[18:19], v[18:19], v[34:35]
	s_waitcnt vmcnt(4)
	v_pk_add_f32 v[34:35], v[18:19], v[38:39]
	v_pk_add_f32 v[18:19], v[20:21], v[36:37]
	v_add_f32_e32 v9, 0, v34
	v_pk_add_f32 v[36:37], v[18:19], v[40:41]
	global_load_dwordx4 v[18:21], v0, s[12:13] offset:1024
	global_load_dwordx4 v[22:25], v0, s[14:15] offset:1024
	global_load_dwordx4 v[26:29], v[6:7], off
	global_load_dwordx4 v[30:33], v[6:7], off offset:1024
	v_add_f32_e32 v9, v9, v35
	v_add_f32_e32 v9, v9, v36
	s_waitcnt vmcnt(7)
	v_pk_add_f32 v[6:7], v[50:51], v[42:43]
	v_add_f32_e32 v9, v9, v37
	s_waitcnt vmcnt(6)
	v_pk_add_f32 v[6:7], v[6:7], v[46:47]
	v_pk_add_f32 v[38:39], v[52:53], v[44:45]
	v_add_f32_e32 v9, v9, v6
	v_add_f32_e32 v9, v9, v7
	v_pk_add_f32 v[38:39], v[38:39], v[48:49]
	s_nop 0
	v_add_f32_e32 v9, v9, v38
	v_add_f32_e32 v9, v9, v39
	s_nop 1
	v_add_f32_dpp v9, v9, v9 quad_perm:[1,0,3,2] row_mask:0xf bank_mask:0xf bound_ctrl:1
	s_nop 1
	v_add_f32_dpp v9, v9, v9 quad_perm:[2,3,0,1] row_mask:0xf bank_mask:0xf bound_ctrl:1
	s_nop 1
	v_add_f32_dpp v9, v9, v9 row_half_mirror row_mask:0xf bank_mask:0xf bound_ctrl:1
	s_nop 1
	v_add_f32_dpp v9, v9, v9 row_mirror row_mask:0xf bank_mask:0xf bound_ctrl:1
	s_nop 0
	v_readlane_b32 s12, v9, 16
	v_readlane_b32 s13, v9, 48
	v_readlane_b32 s0, v9, 0
	v_readlane_b32 s1, v9, 32
	v_mov_b32_e32 v40, s12
	v_mov_b32_e32 v41, s13
	v_pk_add_f32 v[40:41], s[0:1], v[40:41]
	s_nop 0
	v_add_f32_e32 v9, v40, v41
	v_mul_f32_e32 v40, 0x3b000000, v9
	v_pk_add_f32 v[50:51], v[34:35], v[40:41] op_sel_hi:[1,0] neg_lo:[0,1] neg_hi:[0,1]
	v_pk_add_f32 v[52:53], v[36:37], v[40:41] op_sel_hi:[1,0] neg_lo:[0,1] neg_hi:[0,1]
	v_pk_mul_f32 v[34:35], v[50:51], v[50:51]
	v_pk_mul_f32 v[36:37], v[52:53], v[52:53]
	v_add_f32_e32 v9, v34, v35
	v_pk_add_f32 v[6:7], v[6:7], v[40:41] op_sel_hi:[1,0] neg_lo:[0,1] neg_hi:[0,1]
	v_add_f32_e32 v9, v9, v36
	v_pk_mul_f32 v[42:43], v[6:7], v[6:7]
	v_add_f32_e32 v9, v9, v37
	v_pk_add_f32 v[54:55], v[38:39], v[40:41] op_sel_hi:[1,0] neg_lo:[0,1] neg_hi:[0,1]
	v_add_f32_e32 v9, v9, v42
	v_pk_mul_f32 v[38:39], v[54:55], v[54:55]
	v_add_f32_e32 v9, v9, v43
	v_add_f32_e32 v9, v9, v38
	v_add_f32_e32 v9, v9, v39
	s_waitcnt vmcnt(5)
	v_pk_mul_f32 v[10:11], v[10:11], v[50:51]
	v_add_f32_dpp v9, v9, v9 quad_perm:[1,0,3,2] row_mask:0xf bank_mask:0xf bound_ctrl:1
	v_pk_mul_f32 v[12:13], v[12:13], v[52:53]
	s_waitcnt vmcnt(3)
	v_pk_mul_f32 v[6:7], v[18:19], v[6:7]
	v_add_f32_dpp v9, v9, v9 quad_perm:[2,3,0,1] row_mask:0xf bank_mask:0xf bound_ctrl:1
	s_nop 1
	v_add_f32_dpp v9, v9, v9 row_half_mirror row_mask:0xf bank_mask:0xf bound_ctrl:1
	s_nop 1
	v_add_f32_dpp v9, v9, v9 row_mirror row_mask:0xf bank_mask:0xf bound_ctrl:1
	s_nop 0
	v_readlane_b32 s12, v9, 16
	v_readlane_b32 s13, v9, 48
	v_readlane_b32 s0, v9, 0
	v_readlane_b32 s1, v9, 32
	v_mov_b32_e32 v34, s12
	v_mov_b32_e32 v35, s13
	v_pk_add_f32 v[34:35], s[0:1], v[34:35]
	s_mov_b32 s12, 0xf800000
	v_add_f32_e32 v9, v34, v35
	v_fmamk_f32 v9, v9, 0x3b000000, v57
	v_mul_f32_e32 v34, 0x4f800000, v9
	v_cmp_gt_f32_e32 vcc, s12, v9
	s_nop 1
	v_cndmask_b32_e32 v9, v9, v34, vcc
	v_sqrt_f32_e32 v34, v9
	s_nop 0
	v_add_u32_e32 v35, -1, v34
	v_fma_f32 v36, -v35, v34, v9
	v_cmp_ge_f32_e64 s[0:1], 0, v36
	v_add_u32_e32 v36, 1, v34
	s_nop 0
	v_cndmask_b32_e64 v35, v34, v35, s[0:1]
	v_fma_f32 v34, -v36, v34, v9
	v_cmp_lt_f32_e64 s[0:1], 0, v34
	s_nop 1
	v_cndmask_b32_e64 v34, v35, v36, s[0:1]
	v_mul_f32_e32 v35, 0x37800000, v34
	v_cndmask_b32_e32 v34, v34, v35, vcc
	v_cmp_class_f32_e32 vcc, v9, v58
	s_nop 1
	v_cndmask_b32_e32 v9, v34, v9, vcc
	v_div_scale_f32 v42, s[0:1], v9, v9, 1.0
	v_rcp_f32_e32 v43, v42
	global_load_dwordx4 v[34:37], v0, s[8:9]
	global_load_dwordx4 v[38:41], v0, s[10:11]
	v_fma_f32 v44, -v42, v43, 1.0
	v_fmac_f32_e32 v43, v44, v43
	v_div_scale_f32 v44, vcc, 1.0, v9, 1.0
	v_mul_f32_e32 v45, v44, v43
	v_fma_f32 v46, -v42, v45, v44
	v_fmac_f32_e32 v45, v46, v43
	v_fma_f32 v42, -v42, v45, v44
	v_div_fmas_f32 v56, v42, v43, v45
	global_load_dwordx4 v[42:45], v0, s[8:9] offset:1024
	global_load_dwordx4 v[46:49], v0, s[10:11] offset:1024
	v_div_fixup_f32 v56, v56, v9, 1.0
	v_pk_fma_f32 v[10:11], v[56:57], v[10:11], v[14:15] op_sel_hi:[0,1,1]
	s_waitcnt vmcnt(5)
	v_pk_add_f32 v[10:11], v[10:11], v[26:27]
	v_pk_fma_f32 v[12:13], v[56:57], v[12:13], v[16:17] op_sel_hi:[0,1,1]
	v_add_f32_e32 v9, 0, v10
	v_add_f32_e32 v9, v9, v11
	v_pk_add_f32 v[12:13], v[12:13], v[28:29]
	v_pk_fma_f32 v[6:7], v[56:57], v[6:7], v[22:23] op_sel_hi:[0,1,1]
	v_add_f32_e32 v9, v9, v12
	v_pk_mul_f32 v[14:15], v[20:21], v[54:55]
	v_add_f32_e32 v9, v9, v13
	s_waitcnt vmcnt(4)
	v_pk_add_f32 v[6:7], v[6:7], v[30:31]
	v_pk_fma_f32 v[14:15], v[56:57], v[14:15], v[24:25] op_sel_hi:[0,1,1]
	v_add_f32_e32 v9, v9, v6
	v_add_f32_e32 v9, v9, v7
	v_pk_add_f32 v[14:15], v[14:15], v[32:33]
	s_nop 0
	v_add_f32_e32 v9, v9, v14
	v_add_f32_e32 v9, v9, v15
	s_nop 1
	v_add_f32_dpp v9, v9, v9 quad_perm:[1,0,3,2] row_mask:0xf bank_mask:0xf bound_ctrl:1
	s_nop 1
	v_add_f32_dpp v9, v9, v9 quad_perm:[2,3,0,1] row_mask:0xf bank_mask:0xf bound_ctrl:1
	s_nop 1
	v_add_f32_dpp v9, v9, v9 row_half_mirror row_mask:0xf bank_mask:0xf bound_ctrl:1
	s_nop 1
	v_add_f32_dpp v9, v9, v9 row_mirror row_mask:0xf bank_mask:0xf bound_ctrl:1
	s_nop 0
	v_readlane_b32 s8, v9, 16
	v_readlane_b32 s9, v9, 48
	v_readlane_b32 s0, v9, 0
	v_readlane_b32 s1, v9, 32
	v_mov_b32_e32 v16, s8
	v_mov_b32_e32 v17, s9
	v_pk_add_f32 v[16:17], s[0:1], v[16:17]
	s_nop 0
	v_add_f32_e32 v9, v16, v17
	v_mul_f32_e32 v16, 0x3b000000, v9
	v_pk_add_f32 v[10:11], v[10:11], v[16:17] op_sel_hi:[1,0] neg_lo:[0,1] neg_hi:[0,1]
	v_pk_add_f32 v[12:13], v[12:13], v[16:17] op_sel_hi:[1,0] neg_lo:[0,1] neg_hi:[0,1]
	v_pk_mul_f32 v[18:19], v[10:11], v[10:11]
	v_pk_mul_f32 v[20:21], v[12:13], v[12:13]
	v_add_f32_e32 v9, v18, v19
	v_pk_add_f32 v[22:23], v[6:7], v[16:17] op_sel_hi:[1,0] neg_lo:[0,1] neg_hi:[0,1]
	v_add_f32_e32 v9, v9, v20
	v_pk_mul_f32 v[6:7], v[22:23], v[22:23]
	v_add_f32_e32 v9, v9, v21
	v_pk_add_f32 v[14:15], v[14:15], v[16:17] op_sel_hi:[1,0] neg_lo:[0,1] neg_hi:[0,1]
	v_add_f32_e32 v6, v9, v6
	v_pk_mul_f32 v[16:17], v[14:15], v[14:15]
	v_add_f32_e32 v6, v6, v7
	v_add_f32_e32 v6, v6, v16
	v_add_f32_e32 v6, v6, v17
	s_nop 1
	v_add_f32_dpp v6, v6, v6 quad_perm:[1,0,3,2] row_mask:0xf bank_mask:0xf bound_ctrl:1
	s_nop 1
	v_add_f32_dpp v6, v6, v6 quad_perm:[2,3,0,1] row_mask:0xf bank_mask:0xf bound_ctrl:1
	s_nop 1
	v_add_f32_dpp v6, v6, v6 row_half_mirror row_mask:0xf bank_mask:0xf bound_ctrl:1
	s_nop 1
	v_add_f32_dpp v6, v6, v6 row_mirror row_mask:0xf bank_mask:0xf bound_ctrl:1
	s_nop 0
	v_readlane_b32 s8, v6, 16
	v_readlane_b32 s9, v6, 48
	v_readlane_b32 s0, v6, 0
	v_readlane_b32 s1, v6, 32
	v_mov_b32_e32 v6, s8
	v_mov_b32_e32 v7, s9
	v_pk_add_f32 v[6:7], s[0:1], v[6:7]
	s_nop 0
	v_add_f32_e32 v6, v6, v7
	v_fmac_f32_e32 v57, 0x3b000000, v6
	v_mul_f32_e32 v6, 0x4f800000, v57
	v_cmp_gt_f32_e32 vcc, s12, v57
	s_nop 1
	v_cndmask_b32_e32 v6, v57, v6, vcc
	v_sqrt_f32_e32 v7, v6
	s_nop 0
	v_add_u32_e32 v9, -1, v7
	v_fma_f32 v16, -v9, v7, v6
	v_cmp_ge_f32_e64 s[0:1], 0, v16
	v_add_u32_e32 v16, 1, v7
	s_nop 0
	v_cndmask_b32_e64 v9, v7, v9, s[0:1]
	v_fma_f32 v7, -v16, v7, v6
	v_cmp_lt_f32_e64 s[0:1], 0, v7
	s_nop 1
	v_cndmask_b32_e64 v7, v9, v16, s[0:1]
	v_mul_f32_e32 v9, 0x37800000, v7
	v_cndmask_b32_e32 v7, v7, v9, vcc
	v_cmp_class_f32_e32 vcc, v6, v58
	v_lshl_add_u64 v[16:17], v[4:5], 0, v[0:1]
	s_nop 0
	v_cndmask_b32_e32 v6, v7, v6, vcc
	v_div_scale_f32 v7, s[0:1], v6, v6, 1.0
	v_rcp_f32_e32 v9, v7
	s_mov_b32 s0, 0x43000000
	v_fma_f32 v0, -v7, v9, 1.0
	v_fmac_f32_e32 v9, v0, v9
	v_div_scale_f32 v0, vcc, 1.0, v6, 1.0
	v_mul_f32_e32 v4, v0, v9
	v_fma_f32 v5, -v7, v4, v0
	v_fmac_f32_e32 v4, v5, v9
	v_fma_f32 v0, -v7, v4, v0
	v_div_fmas_f32 v0, v0, v9, v4
	v_div_fixup_f32 v0, v0, v6, 1.0
	s_waitcnt vmcnt(3)
	v_pk_mul_f32 v[4:5], v[34:35], v[10:11]
	v_pk_mul_f32 v[6:7], v[36:37], v[12:13]
	s_waitcnt vmcnt(2)
	v_pk_fma_f32 v[4:5], v[0:1], v[4:5], v[38:39] op_sel_hi:[0,1,1]
	v_pk_fma_f32 v[6:7], v[0:1], v[6:7], v[40:41] op_sel_hi:[0,1,1]
	s_waitcnt vmcnt(1)
	v_pk_mul_f32 v[10:11], v[42:43], v[22:23]
	v_pk_mul_f32 v[12:13], v[44:45], v[14:15]
	v_fma_mixlo_f16 v9, v4, s0, 0
	s_waitcnt vmcnt(0)
	v_pk_fma_f32 v[10:11], v[0:1], v[10:11], v[46:47] op_sel_hi:[0,1,1]
	v_pk_fma_f32 v[12:13], v[0:1], v[12:13], v[48:49] op_sel_hi:[0,1,1]
	global_store_dwordx4 v[16:17], v[4:7], off sc1
	global_store_dwordx4 v[16:17], v[10:13], off offset:1024 sc1
	v_mul_f32_e32 v0, 0x43000000, v4
	v_fma_mixlo_f16 v4, v4, s0, -v9 op_sel_hi:[0,0,1]
	v_fma_mixlo_f16 v15, v5, s0, 0
	v_pk_mul_f32 v[18:19], v[6:7], s[0:1] op_sel_hi:[1,0]
	v_fma_mixhi_f16 v4, v5, s0, -v15 op_sel_hi:[0,0,1]
	v_cvt_pk_f16_f32 v15, v18, v19
	v_pk_mul_f32 v[20:21], v[12:13], s[0:1] op_sel_hi:[1,0]
	v_cvt_f32_f16_e32 v18, v15
	v_cvt_f32_f16_sdwa v19, v15 dst_sel:DWORD dst_unused:UNUSED_PAD src0_sel:WORD_1
	v_cvt_pk_f16_f32 v17, v20, v21
	v_cvt_f32_f16_e32 v20, v17
	v_cvt_f32_f16_sdwa v21, v17 dst_sel:DWORD dst_unused:UNUSED_PAD src0_sel:WORD_1
	v_fma_mixlo_f16 v14, v10, s0, 0
	v_mul_f32_e32 v9, 0x43000000, v10
	v_fma_mixlo_f16 v10, v10, s0, -v14 op_sel_hi:[0,0,1]
	v_mul_f32_e32 v14, 0x43000000, v5
	v_fma_mixlo_f16 v5, v11, s0, 0
	v_pk_fma_f32 v[6:7], v[6:7], s[0:1], v[18:19] op_sel_hi:[1,0,1] neg_lo:[0,0,1] neg_hi:[0,0,1]
	v_cvt_pk_f16_f32 v14, v0, v14
	v_mul_f32_e32 v0, 0x43000000, v11
	v_fma_mixhi_f16 v10, v11, s0, -v5 op_sel_hi:[0,0,1]
	v_cvt_pk_f16_f32 v5, v6, v7
	v_pk_fma_f32 v[6:7], v[12:13], s[0:1], v[20:21] op_sel_hi:[1,0,1] neg_lo:[0,0,1] neg_hi:[0,0,1]
	v_cvt_pk_f16_f32 v16, v9, v0
	v_cvt_pk_f16_f32 v11, v6, v7
	v_lshl_add_u64 v[6:7], s[6:7], 0, v[2:3]
	v_lshlrev_b32_e32 v0, 1, v8
	v_lshl_add_u64 v[2:3], s[2:3], 0, v[2:3]
	v_lshl_add_u64 v[6:7], v[6:7], 0, v[0:1]
	v_lshl_add_u64 v[0:1], v[2:3], 0, v[0:1]
	global_store_dwordx2 v[6:7], v[14:15], off sc1
	global_store_dwordx2 v[6:7], v[16:17], off offset:512 sc1
	global_store_dwordx2 v[0:1], v[4:5], off sc1
	global_store_dwordx2 v[0:1], v[10:11], off offset:512 sc1
	s_endpgm
	s_endpgm
	s_endpgm
	s_endpgm
	s_endpgm
	s_endpgm
	s_endpgm
	s_endpgm
	s_endpgm
	s_endpgm
	s_endpgm
	s_endpgm
	s_endpgm
	s_endpgm
	s_endpgm
	s_endpgm
	s_endpgm
	s_endpgm
	s_endpgm
	s_endpgm
	s_endpgm
	s_endpgm
	s_endpgm
	s_endpgm
	s_endpgm
	s_endpgm
	s_endpgm
	s_endpgm
	s_endpgm

.LBB19_5:
	v_lshlrev_b32_e32 v0, 2, v0
	v_and_b32_e32 v50, 0xfc, v0
	v_lshlrev_b64 v[2:3], 11, v[2:3]
	v_lshlrev_b32_e32 v4, 2, v50
	v_mov_b32_e32 v5, 0
	s_waitcnt lgkmcnt(0)
	v_lshl_add_u64 v[2:3], s[14:15], 0, v[2:3]
	v_lshlrev_b64 v[36:37], 11, v[6:7]
	v_lshl_add_u64 v[2:3], v[2:3], 0, v[4:5]
	v_lshl_add_u64 v[0:1], s[18:19], 0, v[36:37]
	global_load_dwordx4 v[8:11], v[2:3], off
	global_load_dwordx4 v[12:15], v4, s[16:17]
	global_load_dwordx4 v[16:19], v4, s[16:17] offset:1024
	global_load_dwordx4 v[20:23], v[2:3], off offset:1024
	v_lshl_add_u64 v[38:39], v[0:1], 0, v[4:5]
	global_load_dwordx4 v[24:27], v[38:39], off
	global_load_dwordx4 v[28:31], v[38:39], off offset:1024
	global_load_dwordx4 v[32:35], v4, s[4:5]
	global_load_dwordx4 v[0:3], v4, s[4:5] offset:1024
	v_lshl_add_u64 v[36:37], s[8:9], 0, v[36:37]
	v_lshl_add_u64 v[48:49], v[36:37], 0, v[4:5]
	global_load_dwordx4 v[36:39], v4, s[6:7]
	global_load_dwordx4 v[40:43], v4, s[6:7] offset:1024
	v_lshlrev_b64 v[6:7], 10, v[6:7]
	v_lshl_add_u64 v[44:45], s[10:11], 0, v[6:7]
	v_lshl_add_u64 v[46:47], s[2:3], 0, v[6:7]
	v_mov_b32_e32 v51, 0x3727c5ac
	s_mov_b32 s5, 0xf800000
	v_mov_b32_e32 v52, 0x260
	s_mov_b32 s4, 0x43000000
	v_lshlrev_b32_e32 v4, 1, v50
	v_lshl_add_u64 v[44:45], v[44:45], 0, v[4:5]
	s_waitcnt vmcnt(8)
	v_pk_add_f32 v[6:7], v[12:13], v[8:9]
	s_waitcnt vmcnt(5)
	v_pk_add_f32 v[6:7], v[24:25], v[6:7]
	v_pk_add_f32 v[8:9], v[14:15], v[10:11]
	v_add_f32_e32 v14, 0, v6
	v_pk_add_f32 v[8:9], v[26:27], v[8:9]
	v_add_f32_e32 v14, v14, v7
	v_pk_add_f32 v[10:11], v[16:17], v[20:21]
	v_add_f32_e32 v14, v14, v8
	s_waitcnt vmcnt(4)
	v_pk_add_f32 v[10:11], v[28:29], v[10:11]
	v_add_f32_e32 v14, v14, v9
	v_pk_add_f32 v[12:13], v[18:19], v[22:23]
	v_add_f32_e32 v14, v14, v10
	v_pk_add_f32 v[12:13], v[30:31], v[12:13]
	v_add_f32_e32 v14, v14, v11
	v_add_f32_e32 v14, v14, v12
	v_add_f32_e32 v14, v14, v13
	s_nop 1
	v_add_f32_dpp v14, v14, v14 quad_perm:[1,0,3,2] row_mask:0xf bank_mask:0xf bound_ctrl:1
	s_nop 1
	v_add_f32_dpp v14, v14, v14 quad_perm:[2,3,0,1] row_mask:0xf bank_mask:0xf bound_ctrl:1
	s_nop 1
	v_add_f32_dpp v14, v14, v14 row_half_mirror row_mask:0xf bank_mask:0xf bound_ctrl:1
	s_nop 1
	v_add_f32_dpp v14, v14, v14 row_mirror row_mask:0xf bank_mask:0xf bound_ctrl:1
	s_nop 0
	v_readlane_b32 s2, v14, 16
	v_readlane_b32 s3, v14, 48
	v_readlane_b32 s0, v14, 0
	v_readlane_b32 s1, v14, 32
	v_mov_b32_e32 v14, s2
	v_mov_b32_e32 v15, s3
	v_pk_add_f32 v[14:15], s[0:1], v[14:15]
	s_nop 0
	v_add_f32_e32 v14, v14, v15
	v_mul_f32_e32 v14, 0x3b000000, v14
	v_pk_add_f32 v[6:7], v[6:7], v[14:15] op_sel_hi:[1,0] neg_lo:[0,1] neg_hi:[0,1]
	v_pk_add_f32 v[8:9], v[8:9], v[14:15] op_sel_hi:[1,0] neg_lo:[0,1] neg_hi:[0,1]
	v_pk_add_f32 v[10:11], v[10:11], v[14:15] op_sel_hi:[1,0] neg_lo:[0,1] neg_hi:[0,1]
	v_pk_add_f32 v[12:13], v[12:13], v[14:15] op_sel_hi:[1,0] neg_lo:[0,1] neg_hi:[0,1]
	v_pk_mul_f32 v[14:15], v[6:7], v[6:7]
	v_pk_mul_f32 v[16:17], v[8:9], v[8:9]
	v_add_f32_e32 v14, v14, v15
	v_add_f32_e32 v14, v14, v16
	v_pk_mul_f32 v[18:19], v[10:11], v[10:11]
	v_add_f32_e32 v14, v14, v17
	v_add_f32_e32 v14, v14, v18
	v_pk_mul_f32 v[20:21], v[12:13], v[12:13]
	v_add_f32_e32 v14, v14, v19
	v_add_f32_e32 v14, v14, v20
	v_add_f32_e32 v14, v14, v21
	s_waitcnt vmcnt(2)
	v_pk_mul_f32 v[10:11], v[0:1], v[10:11]
	v_pk_mul_f32 v[12:13], v[2:3], v[12:13]
	v_add_f32_dpp v14, v14, v14 quad_perm:[1,0,3,2] row_mask:0xf bank_mask:0xf bound_ctrl:1
	v_pk_mul_f32 v[6:7], v[32:33], v[6:7]
	v_pk_mul_f32 v[8:9], v[34:35], v[8:9]
	v_add_f32_dpp v14, v14, v14 quad_perm:[2,3,0,1] row_mask:0xf bank_mask:0xf bound_ctrl:1
	s_nop 1
	v_add_f32_dpp v14, v14, v14 row_half_mirror row_mask:0xf bank_mask:0xf bound_ctrl:1
	s_nop 1
	v_add_f32_dpp v14, v14, v14 row_mirror row_mask:0xf bank_mask:0xf bound_ctrl:1
	s_nop 0
	v_readlane_b32 s2, v14, 16
	v_readlane_b32 s3, v14, 48
	v_readlane_b32 s0, v14, 0
	v_readlane_b32 s1, v14, 32
	v_mov_b32_e32 v14, s2
	v_mov_b32_e32 v15, s3
	v_pk_add_f32 v[14:15], s[0:1], v[14:15]
	s_nop 0
	v_add_f32_e32 v14, v14, v15
	v_fmac_f32_e32 v51, 0x3b000000, v14
	v_mul_f32_e32 v14, 0x4f800000, v51
	v_cmp_gt_f32_e32 vcc, s5, v51
	s_nop 1
	v_cndmask_b32_e32 v14, v51, v14, vcc
	v_sqrt_f32_e32 v15, v14
	s_nop 0
	v_add_u32_e32 v0, -1, v15
	v_add_u32_e32 v1, 1, v15
	v_fma_f32 v16, -v0, v15, v14
	v_fma_f32 v17, -v1, v15, v14
	v_cmp_ge_f32_e64 s[0:1], 0, v16
	s_nop 1
	v_cndmask_b32_e64 v0, v15, v0, s[0:1]
	v_cmp_lt_f32_e64 s[0:1], 0, v17
	s_nop 1
	v_cndmask_b32_e64 v0, v0, v1, s[0:1]
	v_mul_f32_e32 v1, 0x37800000, v0
	v_cndmask_b32_e32 v0, v0, v1, vcc
	v_cmp_class_f32_e32 vcc, v14, v52
	s_nop 1
	v_cndmask_b32_e32 v0, v0, v14, vcc
	v_div_scale_f32 v1, s[0:1], v0, v0, 1.0
	v_rcp_f32_e32 v14, v1
	v_div_scale_f32 v2, vcc, 1.0, v0, 1.0
	v_fma_f32 v3, -v1, v14, 1.0
	v_fmac_f32_e32 v14, v3, v14
	v_mul_f32_e32 v3, v2, v14
	v_fma_f32 v15, -v1, v3, v2
	v_fmac_f32_e32 v3, v15, v14
	v_fma_f32 v1, -v1, v3, v2
	v_div_fmas_f32 v1, v1, v14, v3
	v_div_fixup_f32 v14, v1, v0, 1.0
	s_waitcnt vmcnt(1)
	v_pk_fma_f32 v[0:1], v[14:15], v[6:7], v[36:37] op_sel_hi:[0,1,1]
	v_pk_fma_f32 v[2:3], v[14:15], v[8:9], v[38:39] op_sel_hi:[0,1,1]
	s_waitcnt vmcnt(0)
	v_pk_fma_f32 v[6:7], v[14:15], v[10:11], v[40:41] op_sel_hi:[0,1,1]
	v_pk_fma_f32 v[8:9], v[14:15], v[12:13], v[42:43] op_sel_hi:[0,1,1]
	v_fma_mixlo_f16 v15, v0, s4, 0
	v_pk_mul_f32 v[10:11], v[2:3], s[4:5] op_sel_hi:[1,0]
	global_store_dwordx4 v[48:49], v[0:3], off sc1
	global_store_dwordx4 v[48:49], v[6:9], off offset:1024 sc1
	v_mul_f32_e32 v14, 0x43000000, v0
	v_fma_mixlo_f16 v17, v6, s4, 0
	v_pk_mul_f32 v[12:13], v[8:9], s[4:5] op_sel_hi:[1,0]
	v_fma_mixlo_f16 v0, v0, s4, -v15 op_sel_hi:[0,0,1]
	v_cvt_pk_f16_f32 v15, v10, v11
	v_mul_f32_e32 v16, 0x43000000, v6
	v_fma_mixlo_f16 v6, v6, s4, -v17 op_sel_hi:[0,0,1]
	v_cvt_pk_f16_f32 v17, v12, v13
	v_cvt_f32_f16_e32 v10, v15
	v_cvt_f32_f16_sdwa v11, v15 dst_sel:DWORD dst_unused:UNUSED_PAD src0_sel:WORD_1
	v_cvt_f32_f16_e32 v12, v17
	v_cvt_f32_f16_sdwa v13, v17 dst_sel:DWORD dst_unused:UNUSED_PAD src0_sel:WORD_1
	v_mul_f32_e32 v18, 0x43000000, v1
	v_fma_mixlo_f16 v19, v1, s4, 0
	v_pk_fma_f32 v[2:3], v[2:3], s[4:5], v[10:11] op_sel_hi:[1,0,1] neg_lo:[0,0,1] neg_hi:[0,0,1]
	v_mul_f32_e32 v20, 0x43000000, v7
	v_fma_mixlo_f16 v21, v7, s4, 0
	v_cvt_pk_f16_f32 v14, v14, v18
	v_fma_mixhi_f16 v0, v1, s4, -v19 op_sel_hi:[0,0,1]
	v_pk_fma_f32 v[8:9], v[8:9], s[4:5], v[12:13] op_sel_hi:[1,0,1] neg_lo:[0,0,1] neg_hi:[0,0,1]
	v_cvt_pk_f16_f32 v1, v2, v3
	v_lshl_add_u64 v[2:3], v[46:47], 0, v[4:5]
	v_cvt_pk_f16_f32 v16, v16, v20
	v_fma_mixhi_f16 v6, v7, s4, -v21 op_sel_hi:[0,0,1]
	global_store_dwordx2 v[44:45], v[14:15], off sc1
	global_store_dwordx2 v[44:45], v[16:17], off offset:512 sc1
	v_cvt_pk_f16_f32 v7, v8, v9
	global_store_dwordx2 v[2:3], v[0:1], off sc1
	global_store_dwordx2 v[2:3], v[6:7], off offset:512 sc1
	s_endpgm
	s_endpgm
	s_endpgm
	s_endpgm
	s_endpgm
	s_endpgm
	s_endpgm
	s_endpgm
	s_endpgm
	s_endpgm
	s_endpgm
	s_endpgm

.LBB20_5:
	v_lshlrev_b32_e32 v0, 2, v0
	s_load_dwordx2 s[0:1], s[0:1], 0x8
	v_and_b32_e32 v54, 0xfc, v0
	v_lshlrev_b64 v[44:45], 11, v[2:3]
	v_lshlrev_b64 v[4:5], 11, v[4:5]
	s_waitcnt lgkmcnt(0)
	v_lshl_add_u64 v[24:25], s[18:19], 0, v[44:45]
	v_lshlrev_b32_e32 v0, 2, v54
	v_mov_b32_e32 v1, 0
	v_lshl_add_u64 v[4:5], s[14:15], 0, v[4:5]
	v_lshl_add_u64 v[20:21], v[4:5], 0, v[0:1]
	v_lshl_add_u64 v[26:27], v[24:25], 0, v[0:1]
	global_load_dwordx4 v[4:7], v[20:21], off
	global_load_dwordx4 v[8:11], v0, s[16:17]
	global_load_dwordx4 v[12:15], v0, s[16:17] offset:1024
	global_load_dwordx4 v[16:19], v[20:21], off offset:1024
	v_lshl_add_u64 v[28:29], s[0:1], 2, v[24:25]
	global_load_dwordx4 v[20:23], v[26:27], off
	v_lshl_add_u64 v[46:47], v[28:29], 0, v[0:1]
	global_load_dwordx4 v[24:27], v[26:27], off offset:1024
	s_nop 0
	global_load_dwordx4 v[28:31], v[46:47], off
	global_load_dwordx4 v[32:35], v[46:47], off offset:1024
	global_load_dwordx4 v[36:39], v0, s[8:9]
	global_load_dwordx4 v[40:43], v0, s[8:9] offset:1024
	v_lshl_add_u64 v[44:45], s[4:5], 0, v[44:45]
	v_lshl_add_u64 v[52:53], v[44:45], 0, v[0:1]
	global_load_dwordx4 v[44:47], v0, s[10:11]
	global_load_dwordx4 v[48:51], v0, s[10:11] offset:1024
	v_mov_b32_e32 v55, 0x3727c5ac
	s_mov_b32 s9, 0xf800000
	v_mov_b32_e32 v56, 0x260
	s_mov_b32 s8, 0x43000000
	v_lshlrev_b64 v[2:3], 10, v[2:3]
	s_waitcnt vmcnt(10)
	v_pk_add_f32 v[4:5], v[8:9], v[4:5]
	v_pk_add_f32 v[6:7], v[10:11], v[6:7]
	s_waitcnt vmcnt(8)
	v_pk_add_f32 v[8:9], v[12:13], v[16:17]
	v_pk_add_f32 v[10:11], v[14:15], v[18:19]
	s_waitcnt vmcnt(7)
	v_pk_add_f32 v[4:5], v[4:5], v[20:21]
	v_pk_add_f32 v[6:7], v[6:7], v[22:23]
	s_waitcnt vmcnt(5)
	v_pk_add_f32 v[4:5], v[4:5], v[28:29]
	v_pk_add_f32 v[6:7], v[6:7], v[30:31]
	v_add_f32_e32 v0, 0, v4
	v_add_f32_e32 v0, v0, v5
	v_pk_add_f32 v[8:9], v[8:9], v[24:25]
	v_add_f32_e32 v0, v0, v6
	s_waitcnt vmcnt(4)
	v_pk_add_f32 v[8:9], v[8:9], v[32:33]
	v_add_f32_e32 v0, v0, v7
	v_pk_add_f32 v[10:11], v[10:11], v[26:27]
	v_add_f32_e32 v0, v0, v8
	v_pk_add_f32 v[10:11], v[10:11], v[34:35]
	v_add_f32_e32 v0, v0, v9
	v_add_f32_e32 v0, v0, v10
	v_add_f32_e32 v0, v0, v11
	s_nop 1
	v_add_f32_dpp v0, v0, v0 quad_perm:[1,0,3,2] row_mask:0xf bank_mask:0xf bound_ctrl:1
	s_nop 1
	v_add_f32_dpp v0, v0, v0 quad_perm:[2,3,0,1] row_mask:0xf bank_mask:0xf bound_ctrl:1
	s_nop 1
	v_add_f32_dpp v0, v0, v0 row_half_mirror row_mask:0xf bank_mask:0xf bound_ctrl:1
	s_nop 1
	v_add_f32_dpp v0, v0, v0 row_mirror row_mask:0xf bank_mask:0xf bound_ctrl:1
	s_nop 0
	v_readlane_b32 s4, v0, 16
	v_readlane_b32 s5, v0, 48
	v_readlane_b32 s0, v0, 0
	v_readlane_b32 s1, v0, 32
	v_mov_b32_e32 v12, s4
	v_mov_b32_e32 v13, s5
	v_pk_add_f32 v[12:13], s[0:1], v[12:13]
	s_nop 0
	v_add_f32_e32 v0, v12, v13
	v_mul_f32_e32 v0, 0x3b000000, v0
	v_pk_add_f32 v[4:5], v[4:5], v[0:1] op_sel_hi:[1,0] neg_lo:[0,1] neg_hi:[0,1]
	v_pk_add_f32 v[6:7], v[6:7], v[0:1] op_sel_hi:[1,0] neg_lo:[0,1] neg_hi:[0,1]
	v_pk_mul_f32 v[12:13], v[4:5], v[4:5]
	v_pk_add_f32 v[8:9], v[8:9], v[0:1] op_sel_hi:[1,0] neg_lo:[0,1] neg_hi:[0,1]
	v_pk_add_f32 v[10:11], v[10:11], v[0:1] op_sel_hi:[1,0] neg_lo:[0,1] neg_hi:[0,1]
	v_pk_mul_f32 v[14:15], v[6:7], v[6:7]
	v_add_f32_e32 v0, v12, v13
	v_add_f32_e32 v0, v0, v14
	v_pk_mul_f32 v[16:17], v[8:9], v[8:9]
	v_add_f32_e32 v0, v0, v15
	v_add_f32_e32 v0, v0, v16
	v_pk_mul_f32 v[18:19], v[10:11], v[10:11]
	v_add_f32_e32 v0, v0, v17
	v_add_f32_e32 v0, v0, v18
	v_add_f32_e32 v0, v0, v19
	s_waitcnt vmcnt(3)
	v_pk_mul_f32 v[6:7], v[38:39], v[6:7]
	s_waitcnt vmcnt(2)
	v_pk_mul_f32 v[8:9], v[40:41], v[8:9]
	v_add_f32_dpp v0, v0, v0 quad_perm:[1,0,3,2] row_mask:0xf bank_mask:0xf bound_ctrl:1
	v_pk_mul_f32 v[4:5], v[36:37], v[4:5]
	v_pk_mul_f32 v[10:11], v[42:43], v[10:11]
	v_add_f32_dpp v0, v0, v0 quad_perm:[2,3,0,1] row_mask:0xf bank_mask:0xf bound_ctrl:1
	s_nop 1
	v_add_f32_dpp v0, v0, v0 row_half_mirror row_mask:0xf bank_mask:0xf bound_ctrl:1
	s_nop 1
	v_add_f32_dpp v0, v0, v0 row_mirror row_mask:0xf bank_mask:0xf bound_ctrl:1
	s_nop 0
	v_readlane_b32 s4, v0, 16
	v_readlane_b32 s5, v0, 48
	v_readlane_b32 s0, v0, 0
	v_readlane_b32 s1, v0, 32
	v_mov_b32_e32 v12, s4
	v_mov_b32_e32 v13, s5
	v_pk_add_f32 v[12:13], s[0:1], v[12:13]
	s_nop 0
	v_add_f32_e32 v0, v12, v13
	v_fmac_f32_e32 v55, 0x3b000000, v0
	v_mul_f32_e32 v0, 0x4f800000, v55
	v_cmp_gt_f32_e32 vcc, s9, v55
	s_nop 1
	v_cndmask_b32_e32 v0, v55, v0, vcc
	v_sqrt_f32_e32 v12, v0
	s_nop 0
	v_add_u32_e32 v13, -1, v12
	v_add_u32_e32 v14, 1, v12
	v_fma_f32 v15, -v13, v12, v0
	v_fma_f32 v16, -v14, v12, v0
	v_cmp_ge_f32_e64 s[0:1], 0, v15
	s_nop 1
	v_cndmask_b32_e64 v12, v12, v13, s[0:1]
	v_cmp_lt_f32_e64 s[0:1], 0, v16
	s_nop 1
	v_cndmask_b32_e64 v12, v12, v14, s[0:1]
	v_mul_f32_e32 v13, 0x37800000, v12
	v_cndmask_b32_e32 v12, v12, v13, vcc
	v_cmp_class_f32_e32 vcc, v0, v56
	s_nop 1
	v_cndmask_b32_e32 v0, v12, v0, vcc
	v_div_scale_f32 v12, s[0:1], v0, v0, 1.0
	v_rcp_f32_e32 v13, v12
	v_div_scale_f32 v14, vcc, 1.0, v0, 1.0
	v_fma_f32 v15, -v12, v13, 1.0
	v_fmac_f32_e32 v13, v15, v13
	v_mul_f32_e32 v15, v14, v13
	v_fma_f32 v16, -v12, v15, v14
	v_fmac_f32_e32 v15, v16, v13
	v_fma_f32 v12, -v12, v15, v14
	v_div_fmas_f32 v12, v12, v13, v15
	v_div_fixup_f32 v0, v12, v0, 1.0
	s_waitcnt vmcnt(1)
	v_pk_fma_f32 v[6:7], v[0:1], v[6:7], v[46:47] op_sel_hi:[0,1,1]
	s_waitcnt vmcnt(0)
	v_pk_fma_f32 v[8:9], v[0:1], v[8:9], v[48:49] op_sel_hi:[0,1,1]
	v_pk_fma_f32 v[4:5], v[0:1], v[4:5], v[44:45] op_sel_hi:[0,1,1]
	v_mul_f32_e32 v17, 0x43000000, v8
	v_fma_mixlo_f16 v18, v8, s8, 0
	v_mul_f32_e32 v21, 0x43000000, v9
	v_pk_mul_f32 v[12:13], v[6:7], s[8:9] op_sel_hi:[1,0]
	v_pk_fma_f32 v[10:11], v[0:1], v[10:11], v[50:51] op_sel_hi:[0,1,1]
	global_store_dwordx4 v[52:53], v[4:7], off sc1
	global_store_dwordx4 v[52:53], v[8:11], off offset:1024 sc1
	v_mul_f32_e32 v0, 0x43000000, v4
	v_fma_mixlo_f16 v16, v4, s8, 0
	v_fma_mixlo_f16 v8, v8, s8, -v18 op_sel_hi:[0,0,1]
	v_cvt_pk_f16_f32 v18, v17, v21
	v_cvt_pk_f16_f32 v17, v12, v13
	v_mul_f32_e32 v19, 0x43000000, v5
	v_pk_mul_f32 v[14:15], v[10:11], s[8:9] op_sel_hi:[1,0]
	v_cvt_f32_f16_e32 v12, v17
	v_cvt_f32_f16_sdwa v13, v17 dst_sel:DWORD dst_unused:UNUSED_PAD src0_sel:WORD_1
	v_fma_mixlo_f16 v4, v4, s8, -v16 op_sel_hi:[0,0,1]
	v_cvt_pk_f16_f32 v16, v0, v19
	v_cvt_pk_f16_f32 v19, v14, v15
	v_cvt_f32_f16_e32 v14, v19
	v_cvt_f32_f16_sdwa v15, v19 dst_sel:DWORD dst_unused:UNUSED_PAD src0_sel:WORD_1
	v_fma_mixlo_f16 v20, v5, s8, 0
	v_pk_fma_f32 v[6:7], v[6:7], s[8:9], v[12:13] op_sel_hi:[1,0,1] neg_lo:[0,0,1] neg_hi:[0,0,1]
	v_fma_mixhi_f16 v4, v5, s8, -v20 op_sel_hi:[0,0,1]
	v_cvt_pk_f16_f32 v5, v6, v7
	v_lshl_add_u64 v[6:7], s[6:7], 0, v[2:3]
	v_lshlrev_b32_e32 v0, 1, v54
	v_lshl_add_u64 v[2:3], s[2:3], 0, v[2:3]
	v_fma_mixlo_f16 v22, v9, s8, 0
	v_pk_fma_f32 v[10:11], v[10:11], s[8:9], v[14:15] op_sel_hi:[1,0,1] neg_lo:[0,0,1] neg_hi:[0,0,1]
	v_lshl_add_u64 v[6:7], v[6:7], 0, v[0:1]
	v_lshl_add_u64 v[0:1], v[2:3], 0, v[0:1]
	v_fma_mixhi_f16 v8, v9, s8, -v22 op_sel_hi:[0,0,1]
	v_cvt_pk_f16_f32 v9, v10, v11
	global_store_dwordx2 v[6:7], v[16:17], off sc1
	global_store_dwordx2 v[6:7], v[18:19], off offset:512 sc1
	global_store_dwordx2 v[0:1], v[4:5], off sc1
	global_store_dwordx2 v[0:1], v[8:9], off offset:512 sc1
	s_endpgm
	s_endpgm
	s_endpgm
	s_endpgm
	s_endpgm
	s_endpgm
	s_endpgm
	s_endpgm
	s_endpgm
	s_endpgm
	s_endpgm
	s_endpgm
	s_endpgm
	s_endpgm
	s_endpgm
	s_endpgm
	s_endpgm
	s_endpgm
	s_endpgm
	s_endpgm
	s_endpgm
	s_endpgm
	s_endpgm
	s_endpgm
	s_endpgm
	s_endpgm
	s_endpgm
	s_endpgm
	s_endpgm
	s_endpgm
	s_endpgm
	s_endpgm
	s_endpgm
	s_endpgm
	s_endpgm
	s_endpgm
	s_endpgm
	s_endpgm
	s_endpgm
	s_endpgm
	s_endpgm
	s_endpgm
	s_endpgm
	s_endpgm
	s_endpgm
	s_endpgm
	s_endpgm
	s_endpgm
	s_endpgm
	s_endpgm
	s_endpgm
	s_endpgm
	s_endpgm
	s_endpgm

.LBB21_5:
	v_lshlrev_b32_e32 v0, 2, v0
	v_and_b32_e32 v58, 0xfc, v0
	v_lshlrev_b64 v[4:5], 11, v[4:5]
	v_lshlrev_b32_e32 v0, 2, v58
	v_mov_b32_e32 v1, 0
	s_waitcnt lgkmcnt(0)
	v_lshl_add_u64 v[4:5], s[18:19], 0, v[4:5]
	v_lshl_add_u64 v[20:21], v[4:5], 0, v[0:1]
	global_load_dwordx4 v[4:7], v[20:21], off
	global_load_dwordx4 v[8:11], v0, s[16:17]
	global_load_dwordx4 v[12:15], v0, s[16:17] offset:1024
	global_load_dwordx4 v[16:19], v[20:21], off offset:1024
	s_load_dwordx2 s[0:1], s[0:1], 0x8
	v_lshlrev_b64 v[52:53], 11, v[2:3]
	v_lshl_add_u64 v[28:29], s[14:15], 0, v[52:53]
	v_lshl_add_u64 v[24:25], v[28:29], 0, v[0:1]
	v_mov_b32_e32 v59, 0x3727c5ac
	s_waitcnt lgkmcnt(0)
	v_lshl_add_u64 v[20:21], s[0:1], 2, v[28:29]
	v_lshl_add_u64 v[26:27], s[0:1], 3, v[28:29]
	v_lshl_add_u64 v[36:37], v[20:21], 0, v[0:1]
	global_load_dwordx4 v[20:23], v[24:25], off
	v_lshl_add_u64 v[40:41], v[26:27], 0, v[0:1]
	global_load_dwordx4 v[24:27], v[24:25], off offset:1024
	v_mad_u64_u32 v[44:45], s[12:13], s0, 12, v[28:29]
	v_mov_b32_e32 v38, v45
	v_mad_u64_u32 v[42:43], s[0:1], s1, 12, v[38:39]
	global_load_dwordx4 v[28:31], v[36:37], off
	global_load_dwordx4 v[32:35], v[36:37], off offset:1024
	v_mov_b32_e32 v45, v42
	global_load_dwordx4 v[36:39], v[40:41], off
	v_lshl_add_u64 v[54:55], v[44:45], 0, v[0:1]
	global_load_dwordx4 v[40:43], v[40:41], off offset:1024
	s_nop 0
	global_load_dwordx4 v[44:47], v[54:55], off
	global_load_dwordx4 v[48:51], v[54:55], off offset:1024
	v_mov_b32_e32 v60, 0x260
	v_lshlrev_b64 v[2:3], 10, v[2:3]
	s_waitcnt vmcnt(10)
	v_pk_add_f32 v[54:55], v[8:9], v[4:5]
	v_pk_add_f32 v[56:57], v[10:11], v[6:7]
	global_load_dwordx4 v[4:7], v0, s[8:9]
	global_load_dwordx4 v[8:11], v0, s[8:9] offset:1024
	s_waitcnt vmcnt(10)
	v_pk_add_f32 v[16:17], v[12:13], v[16:17]
	v_lshl_add_u64 v[12:13], s[4:5], 0, v[52:53]
	v_pk_add_f32 v[18:19], v[14:15], v[18:19]
	v_lshl_add_u64 v[52:53], v[12:13], 0, v[0:1]
	global_load_dwordx4 v[12:15], v0, s[10:11]
	s_mov_b32 s9, 0xf800000
	s_mov_b32 s8, 0x43000000
	s_waitcnt vmcnt(10)
	v_pk_add_f32 v[20:21], v[54:55], v[20:21]
	v_pk_add_f32 v[22:23], v[56:57], v[22:23]
	s_waitcnt vmcnt(9)
	v_pk_add_f32 v[24:25], v[16:17], v[24:25]
	v_pk_add_f32 v[26:27], v[18:19], v[26:27]
	global_load_dwordx4 v[16:19], v0, s[10:11] offset:1024
	s_waitcnt vmcnt(9)
	v_pk_add_f32 v[20:21], v[20:21], v[28:29]
	v_pk_add_f32 v[22:23], v[22:23], v[30:31]
	s_waitcnt vmcnt(8)
	v_pk_add_f32 v[24:25], v[24:25], v[32:33]
	s_waitcnt vmcnt(7)
	v_pk_add_f32 v[20:21], v[20:21], v[36:37]
	v_pk_add_f32 v[22:23], v[22:23], v[38:39]
	s_waitcnt vmcnt(5)
	v_pk_add_f32 v[20:21], v[20:21], v[44:45]
	v_pk_add_f32 v[22:23], v[22:23], v[46:47]
	v_add_f32_e32 v0, 0, v20
	v_add_f32_e32 v0, v0, v21
	v_pk_add_f32 v[24:25], v[24:25], v[40:41]
	v_add_f32_e32 v0, v0, v22
	v_pk_add_f32 v[26:27], v[26:27], v[34:35]
	s_waitcnt vmcnt(4)
	v_pk_add_f32 v[24:25], v[24:25], v[48:49]
	v_add_f32_e32 v0, v0, v23
	v_pk_add_f32 v[26:27], v[26:27], v[42:43]
	v_add_f32_e32 v0, v0, v24
	v_pk_add_f32 v[26:27], v[26:27], v[50:51]
	v_add_f32_e32 v0, v0, v25
	v_add_f32_e32 v0, v0, v26
	v_add_f32_e32 v0, v0, v27
	s_nop 1
	v_add_f32_dpp v0, v0, v0 quad_perm:[1,0,3,2] row_mask:0xf bank_mask:0xf bound_ctrl:1
	s_nop 1
	v_add_f32_dpp v0, v0, v0 quad_perm:[2,3,0,1] row_mask:0xf bank_mask:0xf bound_ctrl:1
	s_nop 1
	v_add_f32_dpp v0, v0, v0 row_half_mirror row_mask:0xf bank_mask:0xf bound_ctrl:1
	s_nop 1
	v_add_f32_dpp v0, v0, v0 row_mirror row_mask:0xf bank_mask:0xf bound_ctrl:1
	s_nop 0
	v_readlane_b32 s4, v0, 16
	v_readlane_b32 s5, v0, 48
	v_readlane_b32 s0, v0, 0
	v_readlane_b32 s1, v0, 32
	v_mov_b32_e32 v28, s4
	v_mov_b32_e32 v29, s5
	v_pk_add_f32 v[28:29], s[0:1], v[28:29]
	s_nop 0
	v_add_f32_e32 v0, v28, v29
	v_mul_f32_e32 v0, 0x3b000000, v0
	v_pk_add_f32 v[20:21], v[20:21], v[0:1] op_sel_hi:[1,0] neg_lo:[0,1] neg_hi:[0,1]
	v_pk_add_f32 v[22:23], v[22:23], v[0:1] op_sel_hi:[1,0] neg_lo:[0,1] neg_hi:[0,1]
	v_pk_mul_f32 v[28:29], v[20:21], v[20:21]
	v_pk_add_f32 v[24:25], v[24:25], v[0:1] op_sel_hi:[1,0] neg_lo:[0,1] neg_hi:[0,1]
	v_pk_add_f32 v[26:27], v[26:27], v[0:1] op_sel_hi:[1,0] neg_lo:[0,1] neg_hi:[0,1]
	v_pk_mul_f32 v[30:31], v[22:23], v[22:23]
	v_add_f32_e32 v0, v28, v29
	v_add_f32_e32 v0, v0, v30
	v_pk_mul_f32 v[32:33], v[24:25], v[24:25]
	v_add_f32_e32 v0, v0, v31
	v_add_f32_e32 v0, v0, v32
	v_pk_mul_f32 v[34:35], v[26:27], v[26:27]
	v_add_f32_e32 v0, v0, v33
	v_add_f32_e32 v0, v0, v34
	v_add_f32_e32 v0, v0, v35
	s_waitcnt vmcnt(3)
	v_pk_mul_f32 v[4:5], v[4:5], v[20:21]
	v_add_f32_dpp v0, v0, v0 quad_perm:[1,0,3,2] row_mask:0xf bank_mask:0xf bound_ctrl:1
	v_pk_mul_f32 v[6:7], v[6:7], v[22:23]
	s_waitcnt vmcnt(2)
	v_pk_mul_f32 v[8:9], v[8:9], v[24:25]
	v_add_f32_dpp v0, v0, v0 quad_perm:[2,3,0,1] row_mask:0xf bank_mask:0xf bound_ctrl:1
	v_pk_mul_f32 v[10:11], v[10:11], v[26:27]
	s_nop 0
	v_add_f32_dpp v0, v0, v0 row_half_mirror row_mask:0xf bank_mask:0xf bound_ctrl:1
	s_nop 1
	v_add_f32_dpp v0, v0, v0 row_mirror row_mask:0xf bank_mask:0xf bound_ctrl:1
	s_nop 0
	v_readlane_b32 s4, v0, 16
	v_readlane_b32 s5, v0, 48
	v_readlane_b32 s0, v0, 0
	v_readlane_b32 s1, v0, 32
	v_mov_b32_e32 v28, s4
	v_mov_b32_e32 v29, s5
	v_pk_add_f32 v[28:29], s[0:1], v[28:29]
	s_nop 0
	v_add_f32_e32 v0, v28, v29
	v_fmac_f32_e32 v59, 0x3b000000, v0
	v_mul_f32_e32 v0, 0x4f800000, v59
	v_cmp_gt_f32_e32 vcc, s9, v59
	s_nop 1
	v_cndmask_b32_e32 v0, v59, v0, vcc
	v_sqrt_f32_e32 v28, v0
	s_nop 0
	v_add_u32_e32 v20, -1, v28
	v_add_u32_e32 v21, 1, v28
	v_fma_f32 v22, -v20, v28, v0
	v_fma_f32 v23, -v21, v28, v0
	v_cmp_ge_f32_e64 s[0:1], 0, v22
	s_nop 1
	v_cndmask_b32_e64 v20, v28, v20, s[0:1]
	v_cmp_lt_f32_e64 s[0:1], 0, v23
	s_nop 1
	v_cndmask_b32_e64 v20, v20, v21, s[0:1]
	v_mul_f32_e32 v21, 0x37800000, v20
	v_cndmask_b32_e32 v20, v20, v21, vcc
	v_cmp_class_f32_e32 vcc, v0, v60
	s_nop 1
	v_cndmask_b32_e32 v0, v20, v0, vcc
	v_div_scale_f32 v20, s[0:1], v0, v0, 1.0
	v_rcp_f32_e32 v21, v20
	v_div_scale_f32 v22, vcc, 1.0, v0, 1.0
	v_fma_f32 v23, -v20, v21, 1.0
	v_fmac_f32_e32 v21, v23, v21
	v_mul_f32_e32 v23, v22, v21
	v_fma_f32 v24, -v20, v23, v22
	v_fmac_f32_e32 v23, v24, v21
	v_fma_f32 v20, -v20, v23, v22
	v_div_fmas_f32 v20, v20, v21, v23
	v_div_fixup_f32 v0, v20, v0, 1.0
	s_waitcnt vmcnt(1)
	v_pk_fma_f32 v[4:5], v[0:1], v[4:5], v[12:13] op_sel_hi:[0,1,1]
	v_pk_fma_f32 v[6:7], v[0:1], v[6:7], v[14:15] op_sel_hi:[0,1,1]
	s_waitcnt vmcnt(0)
	v_pk_fma_f32 v[8:9], v[0:1], v[8:9], v[16:17] op_sel_hi:[0,1,1]
	v_fma_mixlo_f16 v12, v4, s8, 0
	v_pk_fma_f32 v[10:11], v[0:1], v[10:11], v[18:19] op_sel_hi:[0,1,1]
	global_store_dwordx4 v[52:53], v[4:7], off sc1
	global_store_dwordx4 v[52:53], v[8:11], off offset:1024 sc1
	v_mul_f32_e32 v0, 0x43000000, v4
	v_fma_mixlo_f16 v4, v4, s8, -v12 op_sel_hi:[0,0,1]
	v_fma_mixlo_f16 v12, v8, s8, 0
	v_mul_f32_e32 v13, 0x43000000, v8
	v_fma_mixlo_f16 v8, v8, s8, -v12 op_sel_hi:[0,0,1]
	v_mul_f32_e32 v12, 0x43000000, v5
	v_fma_mixlo_f16 v14, v5, s8, 0
	v_cvt_pk_f16_f32 v12, v0, v12
	v_mul_f32_e32 v0, 0x43000000, v9
	v_pk_mul_f32 v[16:17], v[6:7], s[8:9] op_sel_hi:[1,0]
	v_fma_mixhi_f16 v4, v5, s8, -v14 op_sel_hi:[0,0,1]
	v_cvt_pk_f16_f32 v14, v13, v0
	v_cvt_pk_f16_f32 v13, v16, v17
	v_pk_mul_f32 v[18:19], v[10:11], s[8:9] op_sel_hi:[1,0]
	v_cvt_f32_f16_e32 v16, v13
	v_cvt_f32_f16_sdwa v17, v13 dst_sel:DWORD dst_unused:UNUSED_PAD src0_sel:WORD_1
	v_cvt_pk_f16_f32 v15, v18, v19
	v_cvt_f32_f16_e32 v18, v15
	v_cvt_f32_f16_sdwa v19, v15 dst_sel:DWORD dst_unused:UNUSED_PAD src0_sel:WORD_1
	v_fma_mixlo_f16 v5, v9, s8, 0
	v_pk_fma_f32 v[6:7], v[6:7], s[8:9], v[16:17] op_sel_hi:[1,0,1] neg_lo:[0,0,1] neg_hi:[0,0,1]
	v_fma_mixhi_f16 v8, v9, s8, -v5 op_sel_hi:[0,0,1]
	v_cvt_pk_f16_f32 v5, v6, v7
	v_pk_fma_f32 v[6:7], v[10:11], s[8:9], v[18:19] op_sel_hi:[1,0,1] neg_lo:[0,0,1] neg_hi:[0,0,1]
	v_lshlrev_b32_e32 v0, 1, v58
	v_cvt_pk_f16_f32 v9, v6, v7
	v_lshl_add_u64 v[6:7], s[6:7], 0, v[2:3]
	v_lshl_add_u64 v[2:3], s[2:3], 0, v[2:3]
	v_lshl_add_u64 v[6:7], v[6:7], 0, v[0:1]
	v_lshl_add_u64 v[0:1], v[2:3], 0, v[0:1]
	global_store_dwordx2 v[6:7], v[12:13], off sc1
	global_store_dwordx2 v[6:7], v[14:15], off offset:512 sc1
	global_store_dwordx2 v[0:1], v[4:5], off sc1
	global_store_dwordx2 v[0:1], v[8:9], off offset:512 sc1
	s_endpgm
	s_endpgm
	s_endpgm
	s_endpgm
	s_endpgm
	s_endpgm
	s_endpgm
	s_endpgm
	s_endpgm
	s_endpgm
	s_endpgm
	s_endpgm
	s_endpgm

.LBB22_5:
	v_lshlrev_b32_e32 v0, 2, v0
	v_and_b32_e32 v66, 0xfc, v0
	v_lshlrev_b64 v[4:5], 11, v[4:5]
	v_lshlrev_b32_e32 v0, 2, v66
	v_mov_b32_e32 v1, 0
	s_waitcnt lgkmcnt(0)
	v_lshl_add_u64 v[4:5], s[18:19], 0, v[4:5]
	v_lshl_add_u64 v[20:21], v[4:5], 0, v[0:1]
	global_load_dwordx4 v[4:7], v[20:21], off
	global_load_dwordx4 v[8:11], v0, s[16:17]
	global_load_dwordx4 v[12:15], v0, s[16:17] offset:1024
	global_load_dwordx4 v[16:19], v[20:21], off offset:1024
	v_lshlrev_b64 v[48:49], 11, v[2:3]
	v_lshl_add_u64 v[40:41], s[14:15], 0, v[48:49]
	v_lshl_add_u64 v[28:29], v[40:41], 0, v[0:1]
	global_load_dwordx4 v[20:23], v[28:29], off
	global_load_dwordx4 v[24:27], v[28:29], off offset:1024
	s_load_dwordx2 s[0:1], s[0:1], 0x8
	v_lshlrev_b64 v[2:3], 10, v[2:3]
	s_waitcnt lgkmcnt(0)
	v_lshl_add_u64 v[28:29], s[0:1], 2, v[40:41]
	v_lshl_add_u64 v[42:43], v[28:29], 0, v[0:1]
	v_mad_u64_u32 v[36:37], s[12:13], s0, 12, v[40:41]
	v_lshl_add_u64 v[32:33], s[0:1], 3, v[40:41]
	global_load_dwordx4 v[28:31], v[42:43], off
	v_mov_b32_e32 v38, v37
	v_lshl_add_u64 v[44:45], v[32:33], 0, v[0:1]
	v_mad_u64_u32 v[38:39], s[12:13], s1, 12, v[38:39]
	global_load_dwordx4 v[32:35], v[44:45], off
	v_mov_b32_e32 v37, v38
	v_lshl_add_u64 v[46:47], v[36:37], 0, v[0:1]
	global_load_dwordx4 v[36:39], v[46:47], off
	v_mad_u64_u32 v[52:53], s[12:13], s0, 20, v[40:41]
	v_mad_u64_u32 v[54:55], s[12:13], s0, 24, v[40:41]
	v_lshl_add_u64 v[50:51], s[0:1], 4, v[40:41]
	v_mad_u64_u32 v[40:41], s[12:13], s0, 28, v[40:41]
	v_lshl_add_u64 v[50:51], v[50:51], 0, v[0:1]
	s_waitcnt vmcnt(7)
	v_pk_add_f32 v[56:57], v[8:9], v[4:5]
	v_mov_b32_e32 v4, v53
	v_pk_add_f32 v[58:59], v[10:11], v[6:7]
	v_mov_b32_e32 v6, v55
	v_mad_u64_u32 v[10:11], s[12:13], s1, 20, v[4:5]
	s_waitcnt vmcnt(5)
	v_pk_add_f32 v[60:61], v[12:13], v[16:17]
	v_mov_b32_e32 v8, v41
	v_mad_u64_u32 v[12:13], s[12:13], s1, 24, v[6:7]
	v_mov_b32_e32 v53, v10
	v_pk_add_f32 v[62:63], v[14:15], v[18:19]
	v_mad_u64_u32 v[14:15], s[0:1], s1, 28, v[8:9]
	global_load_dwordx4 v[4:7], v[50:51], off
	v_mov_b32_e32 v55, v12
	v_lshl_add_u64 v[52:53], v[52:53], 0, v[0:1]
	v_mov_b32_e32 v41, v14
	v_lshl_add_u64 v[54:55], v[54:55], 0, v[0:1]
	global_load_dwordx4 v[12:15], v[52:53], off
	v_lshl_add_u64 v[64:65], v[40:41], 0, v[0:1]
	global_load_dwordx4 v[16:19], v[54:55], off
	global_load_dwordx4 v[8:11], v[42:43], off offset:1024
	s_waitcnt vmcnt(8)
	v_pk_add_f32 v[40:41], v[56:57], v[20:21]
	v_pk_add_f32 v[42:43], v[58:59], v[22:23]
	global_load_dwordx4 v[20:23], v[64:65], off
	s_waitcnt vmcnt(8)
	v_pk_add_f32 v[56:57], v[60:61], v[24:25]
	v_pk_add_f32 v[58:59], v[62:63], v[26:27]
	s_waitcnt vmcnt(7)
	v_pk_add_f32 v[40:41], v[40:41], v[28:29]
	v_pk_add_f32 v[42:43], v[42:43], v[30:31]
	global_load_dwordx4 v[24:27], v[44:45], off offset:1024
	global_load_dwordx4 v[28:31], v[46:47], off offset:1024
	s_waitcnt vmcnt(8)
	v_pk_add_f32 v[44:45], v[40:41], v[32:33]
	v_pk_add_f32 v[46:47], v[42:43], v[34:35]
	global_load_dwordx4 v[32:35], v[50:51], off offset:1024
	global_load_dwordx4 v[40:43], v[52:53], off offset:1024
	s_waitcnt vmcnt(9)
	v_pk_add_f32 v[50:51], v[44:45], v[36:37]
	v_pk_add_f32 v[52:53], v[46:47], v[38:39]
	global_load_dwordx4 v[36:39], v[54:55], off offset:1024
	global_load_dwordx4 v[44:47], v[64:65], off offset:1024
	s_waitcnt vmcnt(10)
	v_pk_add_f32 v[4:5], v[50:51], v[4:5]
	v_pk_add_f32 v[6:7], v[52:53], v[6:7]
	s_waitcnt vmcnt(9)
	v_pk_add_f32 v[50:51], v[4:5], v[12:13]
	v_pk_add_f32 v[52:53], v[6:7], v[14:15]
	global_load_dwordx4 v[4:7], v0, s[8:9]
	global_load_dwordx4 v[12:15], v0, s[10:11]
	s_waitcnt vmcnt(10)
	v_pk_add_f32 v[16:17], v[50:51], v[16:17]
	v_pk_add_f32 v[18:19], v[52:53], v[18:19]
	s_waitcnt vmcnt(9)
	v_pk_add_f32 v[8:9], v[56:57], v[8:9]
	s_waitcnt vmcnt(8)
	v_pk_add_f32 v[50:51], v[16:17], v[20:21]
	v_pk_add_f32 v[52:53], v[18:19], v[22:23]
	global_load_dwordx4 v[16:19], v0, s[8:9] offset:1024
	global_load_dwordx4 v[20:23], v0, s[10:11] offset:1024
	v_pk_add_f32 v[10:11], v[58:59], v[10:11]
	s_waitcnt vmcnt(9)
	v_pk_add_f32 v[8:9], v[8:9], v[24:25]
	v_add_f32_e32 v24, 0, v50
	s_waitcnt vmcnt(8)
	v_pk_add_f32 v[8:9], v[8:9], v[28:29]
	v_pk_add_f32 v[10:11], v[10:11], v[26:27]
	s_waitcnt vmcnt(7)
	v_pk_add_f32 v[8:9], v[8:9], v[32:33]
	v_add_f32_e32 v24, v24, v51
	s_waitcnt vmcnt(6)
	v_pk_add_f32 v[8:9], v[8:9], v[40:41]
	v_pk_add_f32 v[10:11], v[10:11], v[30:31]
	v_add_f32_e32 v24, v24, v52
	s_waitcnt vmcnt(5)
	v_pk_add_f32 v[8:9], v[8:9], v[36:37]
	v_pk_add_f32 v[10:11], v[10:11], v[34:35]
	v_add_f32_e32 v24, v24, v53
	s_waitcnt vmcnt(4)
	v_pk_add_f32 v[8:9], v[8:9], v[44:45]
	v_pk_add_f32 v[10:11], v[10:11], v[42:43]
	v_add_f32_e32 v24, v24, v8
	v_pk_add_f32 v[10:11], v[10:11], v[38:39]
	v_add_f32_e32 v24, v24, v9
	v_pk_add_f32 v[10:11], v[10:11], v[46:47]
	s_nop 0
	v_add_f32_e32 v24, v24, v10
	v_add_f32_e32 v24, v24, v11
	s_nop 1
	v_add_f32_dpp v24, v24, v24 quad_perm:[1,0,3,2] row_mask:0xf bank_mask:0xf bound_ctrl:1
	s_nop 1
	v_add_f32_dpp v24, v24, v24 quad_perm:[2,3,0,1] row_mask:0xf bank_mask:0xf bound_ctrl:1
	s_nop 1
	v_add_f32_dpp v24, v24, v24 row_half_mirror row_mask:0xf bank_mask:0xf bound_ctrl:1
	s_nop 1
	v_add_f32_dpp v24, v24, v24 row_mirror row_mask:0xf bank_mask:0xf bound_ctrl:1
	s_nop 0
	v_readlane_b32 s8, v24, 16
	v_readlane_b32 s9, v24, 48
	v_readlane_b32 s0, v24, 0
	v_readlane_b32 s1, v24, 32
	v_mov_b32_e32 v24, s8
	v_mov_b32_e32 v25, s9
	v_pk_add_f32 v[24:25], s[0:1], v[24:25]
	s_nop 0
	v_add_f32_e32 v24, v24, v25
	v_mul_f32_e32 v24, 0x3b000000, v24
	v_pk_add_f32 v[26:27], v[50:51], v[24:25] op_sel_hi:[1,0] neg_lo:[0,1] neg_hi:[0,1]
	v_pk_add_f32 v[30:31], v[52:53], v[24:25] op_sel_hi:[1,0] neg_lo:[0,1] neg_hi:[0,1]
	v_pk_mul_f32 v[28:29], v[26:27], v[26:27]
	v_pk_mul_f32 v[32:33], v[30:31], v[30:31]
	v_add_f32_e32 v28, v28, v29
	v_pk_add_f32 v[8:9], v[8:9], v[24:25] op_sel_hi:[1,0] neg_lo:[0,1] neg_hi:[0,1]
	v_add_f32_e32 v28, v28, v32
	v_pk_mul_f32 v[34:35], v[8:9], v[8:9]
	v_add_f32_e32 v28, v28, v33
	v_pk_add_f32 v[10:11], v[10:11], v[24:25] op_sel_hi:[1,0] neg_lo:[0,1] neg_hi:[0,1]
	v_add_f32_e32 v28, v28, v34
	v_pk_mul_f32 v[24:25], v[10:11], v[10:11]
	v_add_f32_e32 v28, v28, v35
	v_add_f32_e32 v24, v28, v24
	v_add_f32_e32 v24, v24, v25
	s_waitcnt vmcnt(3)
	v_pk_mul_f32 v[4:5], v[4:5], v[26:27]
	v_add_f32_dpp v24, v24, v24 quad_perm:[1,0,3,2] row_mask:0xf bank_mask:0xf bound_ctrl:1
	v_pk_mul_f32 v[6:7], v[6:7], v[30:31]
	s_waitcnt vmcnt(1)
	v_pk_mul_f32 v[8:9], v[16:17], v[8:9]
	v_add_f32_dpp v24, v24, v24 quad_perm:[2,3,0,1] row_mask:0xf bank_mask:0xf bound_ctrl:1
	v_pk_mul_f32 v[10:11], v[18:19], v[10:11]
	s_nop 0
	v_add_f32_dpp v24, v24, v24 row_half_mirror row_mask:0xf bank_mask:0xf bound_ctrl:1
	s_nop 1
	v_add_f32_dpp v24, v24, v24 row_mirror row_mask:0xf bank_mask:0xf bound_ctrl:1
	s_nop 0
	v_readlane_b32 s8, v24, 16
	v_readlane_b32 s9, v24, 48
	v_readlane_b32 s0, v24, 0
	v_readlane_b32 s1, v24, 32
	v_mov_b32_e32 v24, s8
	v_mov_b32_e32 v25, s9
	v_pk_add_f32 v[24:25], s[0:1], v[24:25]
	s_mov_b32 s0, 0xf800000
	v_add_f32_e32 v24, v24, v25
	v_mov_b32_e32 v25, 0x3727c5ac
	v_fmac_f32_e32 v25, 0x3b000000, v24
	v_mul_f32_e32 v24, 0x4f800000, v25
	v_cmp_gt_f32_e32 vcc, s0, v25
	s_nop 1
	v_cndmask_b32_e32 v24, v25, v24, vcc
	v_sqrt_f32_e32 v25, v24
	s_nop 0
	v_add_u32_e32 v28, -1, v25
	v_fma_f32 v29, -v28, v25, v24
	v_cmp_ge_f32_e64 s[0:1], 0, v29
	v_add_u32_e32 v29, 1, v25
	s_nop 0
	v_cndmask_b32_e64 v28, v25, v28, s[0:1]
	v_fma_f32 v25, -v29, v25, v24
	v_cmp_lt_f32_e64 s[0:1], 0, v25
	s_nop 1
	v_cndmask_b32_e64 v25, v28, v29, s[0:1]
	v_mul_f32_e32 v28, 0x37800000, v25
	v_cndmask_b32_e32 v25, v25, v28, vcc
	v_mov_b32_e32 v28, 0x260
	v_cmp_class_f32_e32 vcc, v24, v28
	s_nop 1
	v_cndmask_b32_e32 v28, v25, v24, vcc
	v_div_scale_f32 v29, s[0:1], v28, v28, 1.0
	v_rcp_f32_e32 v32, v29
	v_lshl_add_u64 v[24:25], s[4:5], 0, v[48:49]
	v_lshl_add_u64 v[24:25], v[24:25], 0, v[0:1]
	s_mov_b32 s0, 0x43000000
	v_fma_f32 v0, -v29, v32, 1.0
	v_fmac_f32_e32 v32, v0, v32
	v_div_scale_f32 v0, vcc, 1.0, v28, 1.0
	v_mul_f32_e32 v33, v0, v32
	v_fma_f32 v34, -v29, v33, v0
	v_fmac_f32_e32 v33, v34, v32
	v_fma_f32 v0, -v29, v33, v0
	v_div_fmas_f32 v0, v0, v32, v33
	v_div_fixup_f32 v0, v0, v28, 1.0
	v_pk_fma_f32 v[4:5], v[0:1], v[4:5], v[12:13] op_sel_hi:[0,1,1]
	v_pk_fma_f32 v[6:7], v[0:1], v[6:7], v[14:15] op_sel_hi:[0,1,1]
	s_waitcnt vmcnt(0)
	v_pk_fma_f32 v[8:9], v[0:1], v[8:9], v[20:21] op_sel_hi:[0,1,1]
	v_fma_mixlo_f16 v12, v4, s0, 0
	v_pk_fma_f32 v[10:11], v[0:1], v[10:11], v[22:23] op_sel_hi:[0,1,1]
	global_store_dwordx4 v[24:25], v[4:7], off sc1
	global_store_dwordx4 v[24:25], v[8:11], off offset:1024 sc1
	v_mul_f32_e32 v0, 0x43000000, v4
	v_fma_mixlo_f16 v4, v4, s0, -v12 op_sel_hi:[0,0,1]
	v_fma_mixlo_f16 v12, v8, s0, 0
	v_mul_f32_e32 v13, 0x43000000, v8
	v_fma_mixlo_f16 v8, v8, s0, -v12 op_sel_hi:[0,0,1]
	v_mul_f32_e32 v12, 0x43000000, v5
	v_fma_mixlo_f16 v14, v5, s0, 0
	v_cvt_pk_f16_f32 v12, v0, v12
	v_mul_f32_e32 v0, 0x43000000, v9
	v_pk_mul_f32 v[16:17], v[6:7], s[0:1] op_sel_hi:[1,0]
	v_fma_mixhi_f16 v4, v5, s0, -v14 op_sel_hi:[0,0,1]
	v_cvt_pk_f16_f32 v14, v13, v0
	v_cvt_pk_f16_f32 v13, v16, v17
	v_pk_mul_f32 v[18:19], v[10:11], s[0:1] op_sel_hi:[1,0]
	v_cvt_f32_f16_e32 v16, v13
	v_cvt_f32_f16_sdwa v17, v13 dst_sel:DWORD dst_unused:UNUSED_PAD src0_sel:WORD_1
	v_cvt_pk_f16_f32 v15, v18, v19
	v_cvt_f32_f16_e32 v18, v15
	v_cvt_f32_f16_sdwa v19, v15 dst_sel:DWORD dst_unused:UNUSED_PAD src0_sel:WORD_1
	v_fma_mixlo_f16 v5, v9, s0, 0
	v_pk_fma_f32 v[6:7], v[6:7], s[0:1], v[16:17] op_sel_hi:[1,0,1] neg_lo:[0,0,1] neg_hi:[0,0,1]
	v_fma_mixhi_f16 v8, v9, s0, -v5 op_sel_hi:[0,0,1]
	v_cvt_pk_f16_f32 v5, v6, v7
	v_pk_fma_f32 v[6:7], v[10:11], s[0:1], v[18:19] op_sel_hi:[1,0,1] neg_lo:[0,0,1] neg_hi:[0,0,1]
	v_lshlrev_b32_e32 v0, 1, v66
	v_cvt_pk_f16_f32 v9, v6, v7
	v_lshl_add_u64 v[6:7], s[6:7], 0, v[2:3]
	v_lshl_add_u64 v[2:3], s[2:3], 0, v[2:3]
	v_lshl_add_u64 v[6:7], v[6:7], 0, v[0:1]
	v_lshl_add_u64 v[0:1], v[2:3], 0, v[0:1]
	global_store_dwordx2 v[6:7], v[12:13], off sc1
	global_store_dwordx2 v[6:7], v[14:15], off offset:512 sc1
	global_store_dwordx2 v[0:1], v[4:5], off sc1
	global_store_dwordx2 v[0:1], v[8:9], off offset:512 sc1
	s_endpgm
	s_endpgm
	s_endpgm
	s_endpgm
	s_endpgm
	s_endpgm
	s_endpgm
	s_endpgm
	s_endpgm
	s_endpgm
	s_endpgm
	s_endpgm
	s_endpgm
	s_endpgm
	s_endpgm
	s_endpgm
	s_endpgm
	s_endpgm
	s_endpgm
	s_endpgm
	s_endpgm
	s_endpgm
	s_endpgm
	s_endpgm
	s_endpgm
	s_endpgm
	s_endpgm
	s_endpgm
	s_endpgm
	s_endpgm
	s_endpgm
	s_endpgm
	s_endpgm
	s_endpgm
	s_endpgm
	s_endpgm
	s_endpgm
	s_endpgm
	s_endpgm
	s_endpgm
	s_endpgm
	s_endpgm
	s_endpgm
	s_endpgm
	s_endpgm
	s_endpgm
	s_endpgm
	s_endpgm
	s_endpgm
	s_endpgm
	s_endpgm
	s_endpgm
	s_endpgm
	s_endpgm
	s_endpgm
	s_endpgm
	s_endpgm
	s_endpgm
